# QKV-epilogue rope re-read and S1 carry scan: L1-bypassing sc1 loads instead of an agent-scope invalidate (which also wiped the XCD L2 under the other workgroups)
# speedup vs baseline: 1.0578x; 1.0102x over previous
.LBB0_1240:
	s_lshl_b64 s[30:31], s[30:31], 1
	s_nop 15
	s_nop 15
	v_mbcnt_lo_u32_b32 v2, -1, 0
	v_mbcnt_hi_u32_b32 v2, -1, v2
	s_add_u32 s30, s50, s30
	v_and_or_b32 v168, v2, 15, s49
	s_addc_u32 s31, s51, s31
	v_lshlrev_b64 v[0:1], 12, v[168:169]
	v_lshl_add_u64 v[0:1], s[30:31], 0, v[0:1]
	v_lshl_add_u64 v[0:1], v[0:1], 0, s[4:5]
	v_and_b32_e32 v168, 48, v2
	v_pk_mul_f32 v[4:5], v[158:159], s[16:17] op_sel_hi:[1,0]
	v_pk_mul_f32 v[2:3], v[156:157], s[16:17] op_sel_hi:[1,0]
	v_lshl_add_u64 v[0:1], v[0:1], 0, v[168:169]
	v_pk_mul_f32 v[6:7], v[154:155], s[16:17] op_sel_hi:[1,0]
	v_pk_mul_f32 v[8:9], v[152:153], s[16:17] op_sel_hi:[1,0]
	v_cvt_pk_bf16_f32 v2, v2, v3
	v_cvt_pk_bf16_f32 v3, v4, v5
	s_mov_b32 s3, 0x10000
	v_cvt_pk_bf16_f32 v4, v8, v9
	v_cvt_pk_bf16_f32 v5, v6, v7
	global_store_dwordx4 v[0:1], v[2:5], off
	v_pk_mul_f32 v[6:7], v[142:143], s[16:17] op_sel_hi:[1,0]
	v_pk_mul_f32 v[8:9], v[140:141], s[16:17] op_sel_hi:[1,0]
	v_pk_mul_f32 v[4:5], v[150:151], s[16:17] op_sel_hi:[1,0]
	v_pk_mul_f32 v[2:3], v[148:149], s[16:17] op_sel_hi:[1,0]
	v_pk_mul_f32 v[10:11], v[124:125], s[16:17] op_sel_hi:[1,0]
	v_cvt_pk_bf16_f32 v2, v2, v3
	v_cvt_pk_bf16_f32 v3, v4, v5
	v_cvt_pk_bf16_f32 v4, v8, v9
	v_cvt_pk_bf16_f32 v5, v6, v7
	global_store_dwordx4 v[0:1], v[2:5], off offset:256
	v_pk_mul_f32 v[6:7], v[138:139], s[16:17] op_sel_hi:[1,0]
	v_pk_mul_f32 v[8:9], v[136:137], s[16:17] op_sel_hi:[1,0]
	v_pk_mul_f32 v[4:5], v[146:147], s[16:17] op_sel_hi:[1,0]
	v_pk_mul_f32 v[2:3], v[144:145], s[16:17] op_sel_hi:[1,0]
	s_cmp_gt_i32 s59, 5
	v_cvt_pk_bf16_f32 v2, v2, v3
	v_cvt_pk_bf16_f32 v3, v4, v5
	v_cvt_pk_bf16_f32 v4, v8, v9
	v_cvt_pk_bf16_f32 v5, v6, v7
	v_add_co_u32_e32 v6, vcc, s3, v0
	v_pk_mul_f32 v[8:9], v[126:127], s[16:17] op_sel_hi:[1,0]
	s_nop 0
	v_addc_co_u32_e32 v7, vcc, 0, v1, vcc
	global_store_dwordx4 v[6:7], v[2:5], off
	s_mov_b32 s3, 0x20000
	s_nop 0
	v_pk_mul_f32 v[4:5], v[134:135], s[16:17] op_sel_hi:[1,0]
	v_pk_mul_f32 v[2:3], v[132:133], s[16:17] op_sel_hi:[1,0]
	s_nop 0
	v_cvt_pk_bf16_f32 v2, v2, v3
	v_cvt_pk_bf16_f32 v3, v4, v5
	v_cvt_pk_bf16_f32 v4, v10, v11
	v_cvt_pk_bf16_f32 v5, v8, v9
	global_store_dwordx4 v[6:7], v[2:5], off offset:256
	v_pk_mul_f32 v[6:7], v[122:123], s[16:17] op_sel_hi:[1,0]
	v_pk_mul_f32 v[8:9], v[120:121], s[16:17] op_sel_hi:[1,0]
	v_pk_mul_f32 v[4:5], v[130:131], s[16:17] op_sel_hi:[1,0]
	v_pk_mul_f32 v[2:3], v[128:129], s[16:17] op_sel_hi:[1,0]
	v_pk_mul_f32 v[10:11], v[108:109], s[16:17] op_sel_hi:[1,0]
	v_cvt_pk_bf16_f32 v2, v2, v3
	v_cvt_pk_bf16_f32 v3, v4, v5
	v_cvt_pk_bf16_f32 v4, v8, v9
	v_cvt_pk_bf16_f32 v5, v6, v7
	v_add_co_u32_e32 v6, vcc, s3, v0
	v_pk_mul_f32 v[8:9], v[110:111], s[16:17] op_sel_hi:[1,0]
	s_nop 0
	v_addc_co_u32_e32 v7, vcc, 0, v1, vcc
	global_store_dwordx4 v[6:7], v[2:5], off
	s_mov_b32 s3, 0x30000
	s_nop 0
	v_pk_mul_f32 v[4:5], v[118:119], s[16:17] op_sel_hi:[1,0]
	v_pk_mul_f32 v[2:3], v[116:117], s[16:17] op_sel_hi:[1,0]
	s_nop 0
	v_cvt_pk_bf16_f32 v2, v2, v3
	v_cvt_pk_bf16_f32 v3, v4, v5
	v_cvt_pk_bf16_f32 v4, v10, v11
	v_cvt_pk_bf16_f32 v5, v8, v9
	global_store_dwordx4 v[6:7], v[2:5], off offset:256
	v_pk_mul_f32 v[6:7], v[106:107], s[16:17] op_sel_hi:[1,0]
	v_pk_mul_f32 v[8:9], v[104:105], s[16:17] op_sel_hi:[1,0]
	v_pk_mul_f32 v[4:5], v[114:115], s[16:17] op_sel_hi:[1,0]
	v_pk_mul_f32 v[2:3], v[112:113], s[16:17] op_sel_hi:[1,0]
	v_pk_mul_f32 v[10:11], v[96:97], s[16:17] op_sel_hi:[1,0]
	v_cvt_pk_bf16_f32 v2, v2, v3
	v_cvt_pk_bf16_f32 v3, v4, v5
	v_cvt_pk_bf16_f32 v4, v8, v9
	v_cvt_pk_bf16_f32 v5, v6, v7
	v_add_co_u32_e32 v6, vcc, s3, v0
	v_pk_mul_f32 v[8:9], v[98:99], s[16:17] op_sel_hi:[1,0]
	s_nop 0
	v_addc_co_u32_e32 v7, vcc, 0, v1, vcc
	global_store_dwordx4 v[6:7], v[2:5], off
	s_mov_b32 s3, 0x80000
	s_nop 0
	v_pk_mul_f32 v[4:5], v[102:103], s[16:17] op_sel_hi:[1,0]
	v_pk_mul_f32 v[2:3], v[100:101], s[16:17] op_sel_hi:[1,0]
	s_nop 0
	v_cvt_pk_bf16_f32 v2, v2, v3
	v_cvt_pk_bf16_f32 v3, v4, v5
	v_cvt_pk_bf16_f32 v4, v10, v11
	v_cvt_pk_bf16_f32 v5, v8, v9
	global_store_dwordx4 v[6:7], v[2:5], off offset:256
	v_pk_mul_f32 v[6:7], v[90:91], s[16:17] op_sel_hi:[1,0]
	v_pk_mul_f32 v[8:9], v[88:89], s[16:17] op_sel_hi:[1,0]
	v_pk_mul_f32 v[4:5], v[94:95], s[16:17] op_sel_hi:[1,0]
	v_pk_mul_f32 v[2:3], v[92:93], s[16:17] op_sel_hi:[1,0]
	v_pk_mul_f32 v[10:11], v[76:77], s[16:17] op_sel_hi:[1,0]
	v_cvt_pk_bf16_f32 v2, v2, v3
	v_cvt_pk_bf16_f32 v3, v4, v5
	v_cvt_pk_bf16_f32 v4, v8, v9
	v_cvt_pk_bf16_f32 v5, v6, v7
	v_add_co_u32_e32 v6, vcc, s3, v0
	v_pk_mul_f32 v[8:9], v[78:79], s[16:17] op_sel_hi:[1,0]
	s_nop 0
	v_addc_co_u32_e32 v7, vcc, 0, v1, vcc
	global_store_dwordx4 v[6:7], v[2:5], off
	s_mov_b32 s3, 0x90000
	s_nop 0
	v_pk_mul_f32 v[4:5], v[86:87], s[16:17] op_sel_hi:[1,0]
	v_pk_mul_f32 v[2:3], v[84:85], s[16:17] op_sel_hi:[1,0]
	s_nop 0
	v_cvt_pk_bf16_f32 v2, v2, v3
	v_cvt_pk_bf16_f32 v3, v4, v5
	v_cvt_pk_bf16_f32 v4, v10, v11
	v_cvt_pk_bf16_f32 v5, v8, v9
	global_store_dwordx4 v[6:7], v[2:5], off offset:256
	v_pk_mul_f32 v[6:7], v[74:75], s[16:17] op_sel_hi:[1,0]
	v_pk_mul_f32 v[8:9], v[72:73], s[16:17] op_sel_hi:[1,0]
	v_pk_mul_f32 v[4:5], v[82:83], s[16:17] op_sel_hi:[1,0]
	v_pk_mul_f32 v[2:3], v[80:81], s[16:17] op_sel_hi:[1,0]
	v_pk_mul_f32 v[10:11], v[60:61], s[16:17] op_sel_hi:[1,0]
	v_cvt_pk_bf16_f32 v2, v2, v3
	v_cvt_pk_bf16_f32 v3, v4, v5
	v_cvt_pk_bf16_f32 v4, v8, v9
	v_cvt_pk_bf16_f32 v5, v6, v7
	v_add_co_u32_e32 v6, vcc, s3, v0
	v_pk_mul_f32 v[8:9], v[62:63], s[16:17] op_sel_hi:[1,0]
	s_nop 0
	v_addc_co_u32_e32 v7, vcc, 0, v1, vcc
	global_store_dwordx4 v[6:7], v[2:5], off
	s_mov_b32 s3, 0xa0000
	s_nop 0
	v_pk_mul_f32 v[4:5], v[70:71], s[16:17] op_sel_hi:[1,0]
	v_pk_mul_f32 v[2:3], v[68:69], s[16:17] op_sel_hi:[1,0]
	s_nop 0
	v_cvt_pk_bf16_f32 v2, v2, v3
	v_cvt_pk_bf16_f32 v3, v4, v5
	v_cvt_pk_bf16_f32 v4, v10, v11
	v_cvt_pk_bf16_f32 v5, v8, v9
	global_store_dwordx4 v[6:7], v[2:5], off offset:256
	v_pk_mul_f32 v[6:7], v[58:59], s[16:17] op_sel_hi:[1,0]
	v_pk_mul_f32 v[8:9], v[56:57], s[16:17] op_sel_hi:[1,0]
	v_pk_mul_f32 v[4:5], v[66:67], s[16:17] op_sel_hi:[1,0]
	v_pk_mul_f32 v[2:3], v[64:65], s[16:17] op_sel_hi:[1,0]
	v_pk_mul_f32 v[10:11], v[44:45], s[16:17] op_sel_hi:[1,0]
	v_cvt_pk_bf16_f32 v2, v2, v3
	v_cvt_pk_bf16_f32 v3, v4, v5
	v_cvt_pk_bf16_f32 v4, v8, v9
	v_cvt_pk_bf16_f32 v5, v6, v7
	v_add_co_u32_e32 v6, vcc, s3, v0
	v_pk_mul_f32 v[8:9], v[46:47], s[16:17] op_sel_hi:[1,0]
	s_nop 0
	v_addc_co_u32_e32 v7, vcc, 0, v1, vcc
	global_store_dwordx4 v[6:7], v[2:5], off
	s_mov_b32 s3, 0xb0000
	s_nop 0
	v_pk_mul_f32 v[4:5], v[54:55], s[16:17] op_sel_hi:[1,0]
	v_pk_mul_f32 v[2:3], v[52:53], s[16:17] op_sel_hi:[1,0]
	s_nop 0
	v_cvt_pk_bf16_f32 v2, v2, v3
	v_cvt_pk_bf16_f32 v3, v4, v5
	v_cvt_pk_bf16_f32 v4, v10, v11
	v_cvt_pk_bf16_f32 v5, v8, v9
	global_store_dwordx4 v[6:7], v[2:5], off offset:256
	v_pk_mul_f32 v[6:7], v[42:43], s[16:17] op_sel_hi:[1,0]
	v_pk_mul_f32 v[8:9], v[40:41], s[16:17] op_sel_hi:[1,0]
	v_pk_mul_f32 v[4:5], v[50:51], s[16:17] op_sel_hi:[1,0]
	v_pk_mul_f32 v[2:3], v[48:49], s[16:17] op_sel_hi:[1,0]
	s_nop 0
	v_cvt_pk_bf16_f32 v2, v2, v3
	v_cvt_pk_bf16_f32 v3, v4, v5
	v_cvt_pk_bf16_f32 v4, v8, v9
	v_cvt_pk_bf16_f32 v5, v6, v7
	v_add_co_u32_e32 v6, vcc, s3, v0
	v_pk_mul_f32 v[8:9], v[32:33], s[16:17] op_sel_hi:[1,0]
	s_nop 0
	v_addc_co_u32_e32 v7, vcc, 0, v1, vcc
	global_store_dwordx4 v[6:7], v[2:5], off
	v_pk_mul_f32 v[0:1], v[36:37], s[16:17] op_sel_hi:[1,0]
	s_nop 0
	v_pk_mul_f32 v[2:3], v[38:39], s[16:17] op_sel_hi:[1,0]
	v_pk_mul_f32 v[4:5], v[34:35], s[16:17] op_sel_hi:[1,0]
	v_cvt_pk_bf16_f32 v0, v0, v1
	v_cvt_pk_bf16_f32 v1, v2, v3
	v_cvt_pk_bf16_f32 v2, v8, v9
	s_nop 0
	v_cvt_pk_bf16_f32 v3, v4, v5
	global_store_dwordx4 v[6:7], v[0:3], off offset:256
	s_cbranch_scc1 .LBB0_1243
	s_waitcnt vmcnt(0)
	s_barrier
	s_waitcnt vmcnt(0)
	s_waitcnt vmcnt(0)
	v_mbcnt_lo_u32_b32 v4, -1, 0
	v_mbcnt_hi_u32_b32 v4, -1, v4
	v_readlane_b32 s60, v253, 43
	v_lshlrev_b32_e32 v0, 1, v4
	v_and_b32_e32 v7, 30, v0
	v_bfe_u32 v6, v4, 4, 1
	s_cmp_lt_i32 s59, 4
	v_readlane_b32 s62, v253, 45
	v_readlane_b32 s63, v253, 46
	v_readlane_b32 s64, v253, 47
	v_readlane_b32 s65, v253, 48
	v_lshlrev_b32_e32 v8, 2, v7
	s_cselect_b32 s35, s63, s65
	s_cselect_b32 s34, s62, s64
	v_lshl_or_b32 v2, v6, 8, v8
	global_load_dwordx2 v[0:1], v2, s[34:35]
	s_nop 0
	global_load_dwordx2 v[2:3], v2, s[34:35] offset:128
	v_lshlrev_b32_e32 v4, 2, v4
	s_add_u32 s30, s30, s14
	v_and_b32_e32 v4, 0xffffff80, v4
	s_addc_u32 s31, s31, s15
	v_ashrrev_i32_e32 v5, 31, v4
	v_lshl_add_u64 v[4:5], v[4:5], 1, s[30:31]
	v_lshlrev_b32_e32 v168, 7, v6
	s_lshl_b32 s2, s2, 8
	v_lshl_add_u64 v[4:5], v[4:5], 0, v[168:169]
	v_lshlrev_b32_e32 v168, 1, v7
	s_add_i32 s19, s2, s12
	v_lshl_add_u64 v[4:5], v[4:5], 0, v[168:169]
	v_cmp_eq_u32_e64 s[2:3], 0, v6
	s_bfe_u32 s19, s19, 0x60006
	v_add_u32_e32 v20, s56, v8
	s_mov_b32 s30, -8
	v_readlane_b32 s61, v253, 44
	v_readlane_b32 s66, v253, 49
	v_readlane_b32 s67, v253, 50
	v_readlane_b32 s68, v253, 51
	v_readlane_b32 s69, v253, 52
	v_readlane_b32 s70, v253, 53
	v_readlane_b32 s71, v253, 54
	v_readlane_b32 s72, v253, 55
	v_readlane_b32 s73, v253, 56
	v_readlane_b32 s74, v253, 57
	v_readlane_b32 s75, v253, 58
.LBB0_1242:
	global_load_dword v21, v[4:5], off sc1
	global_load_dword v22, v[4:5], off offset:64 sc1
	v_add_co_u32_e32 v18, vcc, 0x1000, v4
	s_add_i32 s31, s13, s30
	s_nop 0
	v_addc_co_u32_e32 v19, vcc, 0, v5, vcc
	global_load_dword v24, v[18:19], off sc1
	global_load_dword v25, v[18:19], off offset:64 sc1
	v_add_co_u32_e32 v16, vcc, 0x2000, v4
	s_add_i32 s33, s31, 8
	s_nop 0
	v_addc_co_u32_e32 v17, vcc, 0, v5, vcc
	global_load_dword v26, v[16:17], off sc1
	global_load_dword v27, v[16:17], off offset:64 sc1
	v_add_co_u32_e32 v14, vcc, 0x3000, v4
	v_mov_b32_e32 v23, s33
	s_nop 0
	v_addc_co_u32_e32 v15, vcc, 0, v5, vcc
	global_load_dword v28, v[14:15], off sc1
	global_load_dword v29, v[14:15], off offset:64 sc1
	v_add_co_u32_e32 v12, vcc, 0x4000, v4
	v_mov_b32_e32 v38, s19
	s_nop 0
	v_addc_co_u32_e32 v13, vcc, 0, v5, vcc
	global_load_dword v30, v[12:13], off sc1
	global_load_dword v31, v[12:13], off offset:64 sc1
	v_add_co_u32_e32 v10, vcc, 0x5000, v4
	v_cndmask_b32_e64 v23, v23, v38, s[2:3]
	s_nop 0
	v_addc_co_u32_e32 v11, vcc, 0, v5, vcc
	v_add_co_u32_e32 v8, vcc, 0x6000, v4
	global_load_dword v32, v[10:11], off sc1
	global_load_dword v33, v[10:11], off offset:64 sc1
	v_addc_co_u32_e32 v9, vcc, 0, v5, vcc
	v_add_co_u32_e32 v6, vcc, 0x7000, v4
	global_load_dword v34, v[8:9], off sc1
	global_load_dword v35, v[8:9], off offset:64 sc1
	v_addc_co_u32_e32 v7, vcc, 0, v5, vcc
	global_load_dword v36, v[6:7], off sc1
	global_load_dword v37, v[6:7], off offset:64 sc1
	s_add_i32 s33, s31, 9
	s_add_i32 s30, s30, 8
	s_mov_b64 s[34:35], 0x8000
	s_waitcnt vmcnt(15)
	v_lshlrev_b32_e32 v39, 16, v21
	v_and_b32_e32 v21, 0xffff0000, v21
	s_waitcnt vmcnt(14)
	v_and_b32_e32 v41, 0xffff0000, v22
	v_lshlrev_b32_e32 v40, 16, v22
	v_mul_f32_e32 v22, v21, v21
	v_mul_f32_e32 v42, v41, v41
	v_fmac_f32_e32 v22, v39, v39
	v_fmac_f32_e32 v42, v40, v40
	v_add_f32_e32 v22, v22, v42
	s_nop 1
	v_add_f32_dpp v22, v22, v22 quad_perm:[1,0,3,2] row_mask:0xf bank_mask:0xf bound_ctrl:1
	s_nop 1
	v_add_f32_dpp v22, v22, v22 quad_perm:[2,3,0,1] row_mask:0xf bank_mask:0xf bound_ctrl:1
	s_nop 1
	v_add_f32_dpp v22, v22, v22 row_half_mirror row_mask:0xf bank_mask:0xf bound_ctrl:1
	s_nop 1
	v_add_f32_dpp v22, v22, v22 row_mirror row_mask:0xf bank_mask:0xf bound_ctrl:1
	v_mov_b32_e32 v42, v22
	s_nop 1
	v_permlane16_swap_b32_e32 v22, v42
	v_add_f32_e32 v22, v22, v42
	v_fmamk_f32 v22, v22, 0x3c000000, v186
	v_rsq_f32_e32 v42, v22
	v_lshl_add_u32 v22, v23, 7, v20
	ds_read_b64 v[22:23], v22
	v_mul_f32_e32 v41, v42, v41
	v_mul_f32_e32 v39, v42, v39
	v_mul_f32_e32 v21, v42, v21
	v_mul_f32_e32 v40, v42, v40
	v_mul_f32_e32 v41, v3, v41
	s_waitcnt lgkmcnt(0)
	v_lshlrev_b32_e32 v44, 16, v23
	v_and_b32_e32 v23, 0xffff0000, v23
	v_mul_f32_e32 v39, v0, v39
	v_mul_f32_e32 v21, v1, v21
	v_mul_f32_e32 v40, v2, v40
	v_lshlrev_b32_e32 v42, 16, v22
	v_and_b32_e32 v22, 0xffff0000, v22
	v_mul_f32_e32 v45, v41, v23
	v_mul_f32_e32 v43, v40, v22
	v_fma_f32 v45, v21, v44, -v45
	v_mul_f32_e32 v22, v39, v22
	v_mul_f32_e32 v21, v21, v23
	v_fma_f32 v43, v39, v42, -v43
	v_fmac_f32_e32 v22, v40, v42
	v_fmac_f32_e32 v21, v41, v44
	s_waitcnt vmcnt(13)
	v_lshlrev_b32_e32 v39, 16, v24
	v_and_b32_e32 v24, 0xffff0000, v24
	s_waitcnt vmcnt(12)
	v_lshlrev_b32_e32 v40, 16, v25
	v_and_b32_e32 v25, 0xffff0000, v25
	v_cvt_pk_bf16_f32 v43, v43, v45
	global_store_dword v[4:5], v43, off
	v_cvt_pk_bf16_f32 v21, v22, v21
	v_mul_f32_e32 v22, v24, v24
	v_mul_f32_e32 v23, v25, v25
	v_fmac_f32_e32 v22, v39, v39
	v_fmac_f32_e32 v23, v40, v40
	v_add_f32_e32 v22, v22, v23
	global_store_dword v[4:5], v21, off offset:64
	v_mov_b32_e32 v21, s33
	v_add_f32_dpp v22, v22, v22 quad_perm:[1,0,3,2] row_mask:0xf bank_mask:0xf bound_ctrl:1
	v_cndmask_b32_e64 v21, v21, v38, s[2:3]
	v_lshl_add_u32 v21, v21, 7, v20
	v_add_f32_dpp v22, v22, v22 quad_perm:[2,3,0,1] row_mask:0xf bank_mask:0xf bound_ctrl:1
	s_add_i32 s33, s31, 10
	v_lshl_add_u64 v[4:5], v[4:5], 0, s[34:35]
	v_add_f32_dpp v22, v22, v22 row_half_mirror row_mask:0xf bank_mask:0xf bound_ctrl:1
	s_nop 1
	v_add_f32_dpp v22, v22, v22 row_mirror row_mask:0xf bank_mask:0xf bound_ctrl:1
	v_mov_b32_e32 v23, v22
	s_nop 1
	v_permlane16_swap_b32_e32 v22, v23
	v_add_f32_e32 v22, v22, v23
	v_fmamk_f32 v22, v22, 0x3c000000, v186
	v_rsq_f32_e32 v41, v22
	ds_read_b64 v[22:23], v21
	v_mul_f32_e32 v21, v41, v39
	v_mul_f32_e32 v39, v41, v40
	v_mul_f32_e32 v24, v41, v24
	v_mul_f32_e32 v39, v2, v39
	s_waitcnt lgkmcnt(0)
	v_lshlrev_b32_e32 v40, 16, v22
	v_and_b32_e32 v22, 0xffff0000, v22
	v_mul_f32_e32 v21, v0, v21
	v_mul_f32_e32 v24, v1, v24
	v_mul_f32_e32 v25, v41, v25
	v_mul_f32_e32 v41, v39, v22
	v_lshlrev_b32_e32 v42, 16, v23
	v_and_b32_e32 v23, 0xffff0000, v23
	v_mul_f32_e32 v25, v3, v25
	v_fma_f32 v41, v21, v40, -v41
	v_mul_f32_e32 v21, v21, v22
	v_mul_f32_e32 v22, v24, v23
	v_mul_f32_e32 v43, v25, v23
	v_fmac_f32_e32 v21, v39, v40
	v_fmac_f32_e32 v22, v25, v42
	v_fma_f32 v43, v24, v42, -v43
	v_cvt_pk_bf16_f32 v41, v41, v43
	global_store_dword v[18:19], v41, off
	v_cvt_pk_bf16_f32 v21, v21, v22
	s_waitcnt vmcnt(14)
	v_and_b32_e32 v22, 0xffff0000, v26
	s_waitcnt vmcnt(13)
	v_and_b32_e32 v24, 0xffff0000, v27
	global_store_dword v[18:19], v21, off offset:64
	v_lshlrev_b32_e32 v21, 16, v26
	v_lshlrev_b32_e32 v23, 16, v27
	v_mul_f32_e32 v19, v22, v22
	v_mul_f32_e32 v25, v24, v24
	v_fmac_f32_e32 v19, v21, v21
	v_fmac_f32_e32 v25, v23, v23
	v_add_f32_e32 v19, v19, v25
	v_mov_b32_e32 v18, s33
	v_cndmask_b32_e64 v18, v18, v38, s[2:3]
	v_add_f32_dpp v19, v19, v19 quad_perm:[1,0,3,2] row_mask:0xf bank_mask:0xf bound_ctrl:1
	v_lshl_add_u32 v18, v18, 7, v20
	s_add_i32 s33, s31, 11
	v_add_f32_dpp v19, v19, v19 quad_perm:[2,3,0,1] row_mask:0xf bank_mask:0xf bound_ctrl:1
	s_nop 1
	v_add_f32_dpp v19, v19, v19 row_half_mirror row_mask:0xf bank_mask:0xf bound_ctrl:1
	s_nop 1
	v_add_f32_dpp v19, v19, v19 row_mirror row_mask:0xf bank_mask:0xf bound_ctrl:1
	v_mov_b32_e32 v25, v19
	s_nop 1
	v_permlane16_swap_b32_e32 v19, v25
	v_add_f32_e32 v19, v19, v25
	v_fmamk_f32 v19, v19, 0x3c000000, v186
	v_rsq_f32_e32 v25, v19
	ds_read_b64 v[18:19], v18
	v_mul_f32_e32 v21, v25, v21
	v_mul_f32_e32 v22, v25, v22
	v_mul_f32_e32 v23, v25, v23
	v_mul_f32_e32 v24, v25, v24
	v_mul_f32_e32 v21, v0, v21
	v_mul_f32_e32 v22, v1, v22
	v_mul_f32_e32 v23, v2, v23
	v_mul_f32_e32 v24, v3, v24
	s_waitcnt lgkmcnt(0)
	v_lshlrev_b32_e32 v25, 16, v18
	v_and_b32_e32 v18, 0xffff0000, v18
	v_lshlrev_b32_e32 v27, 16, v19
	v_and_b32_e32 v19, 0xffff0000, v19
	v_mul_f32_e32 v26, v23, v18
	v_mul_f32_e32 v39, v24, v19
	v_mul_f32_e32 v18, v21, v18
	v_mul_f32_e32 v19, v22, v19
	v_fma_f32 v26, v21, v25, -v26
	v_fmac_f32_e32 v18, v23, v25
	v_fmac_f32_e32 v19, v24, v27
	v_fma_f32 v39, v22, v27, -v39
	v_cvt_pk_bf16_f32 v26, v26, v39
	global_store_dword v[16:17], v26, off
	v_cvt_pk_bf16_f32 v18, v18, v19
	s_waitcnt vmcnt(14)
	v_and_b32_e32 v19, 0xffff0000, v28
	s_waitcnt vmcnt(13)
	v_and_b32_e32 v22, 0xffff0000, v29
	global_store_dword v[16:17], v18, off offset:64
	v_lshlrev_b32_e32 v18, 16, v28
	v_lshlrev_b32_e32 v21, 16, v29
	v_mul_f32_e32 v17, v19, v19
	v_mul_f32_e32 v23, v22, v22
	v_fmac_f32_e32 v17, v18, v18
	v_fmac_f32_e32 v23, v21, v21
	v_add_f32_e32 v17, v17, v23
	v_mov_b32_e32 v16, s33
	v_cndmask_b32_e64 v16, v16, v38, s[2:3]
	v_add_f32_dpp v17, v17, v17 quad_perm:[1,0,3,2] row_mask:0xf bank_mask:0xf bound_ctrl:1
	v_lshl_add_u32 v16, v16, 7, v20
	s_add_i32 s33, s31, 12
	v_add_f32_dpp v17, v17, v17 quad_perm:[2,3,0,1] row_mask:0xf bank_mask:0xf bound_ctrl:1
	s_nop 1
	v_add_f32_dpp v17, v17, v17 row_half_mirror row_mask:0xf bank_mask:0xf bound_ctrl:1
	s_nop 1
	v_add_f32_dpp v17, v17, v17 row_mirror row_mask:0xf bank_mask:0xf bound_ctrl:1
	v_mov_b32_e32 v23, v17
	s_nop 1
	v_permlane16_swap_b32_e32 v17, v23
	v_add_f32_e32 v17, v17, v23
	v_fmamk_f32 v17, v17, 0x3c000000, v186
	v_rsq_f32_e32 v23, v17
	ds_read_b64 v[16:17], v16
	v_mul_f32_e32 v18, v23, v18
	v_mul_f32_e32 v19, v23, v19
	v_mul_f32_e32 v21, v23, v21
	v_mul_f32_e32 v22, v23, v22
	v_mul_f32_e32 v18, v0, v18
	v_mul_f32_e32 v19, v1, v19
	v_mul_f32_e32 v21, v2, v21
	v_mul_f32_e32 v22, v3, v22
	s_waitcnt lgkmcnt(0)
	v_lshlrev_b32_e32 v23, 16, v16
	v_and_b32_e32 v16, 0xffff0000, v16
	v_lshlrev_b32_e32 v25, 16, v17
	v_and_b32_e32 v17, 0xffff0000, v17
	v_mul_f32_e32 v24, v21, v16
	v_mul_f32_e32 v26, v22, v17
	v_mul_f32_e32 v16, v18, v16
	v_mul_f32_e32 v17, v19, v17
	v_fma_f32 v24, v18, v23, -v24
	v_fmac_f32_e32 v16, v21, v23
	v_fmac_f32_e32 v17, v22, v25
	v_fma_f32 v26, v19, v25, -v26
	v_cvt_pk_bf16_f32 v24, v24, v26
	global_store_dword v[14:15], v24, off
	v_cvt_pk_bf16_f32 v16, v16, v17
	s_waitcnt vmcnt(14)
	v_and_b32_e32 v17, 0xffff0000, v30
	s_waitcnt vmcnt(13)
	v_and_b32_e32 v19, 0xffff0000, v31
	global_store_dword v[14:15], v16, off offset:64
	v_lshlrev_b32_e32 v16, 16, v30
	v_lshlrev_b32_e32 v18, 16, v31
	v_mul_f32_e32 v15, v17, v17
	v_mul_f32_e32 v21, v19, v19
	v_fmac_f32_e32 v15, v16, v16
	v_fmac_f32_e32 v21, v18, v18
	v_add_f32_e32 v15, v15, v21
	v_mov_b32_e32 v14, s33
	v_cndmask_b32_e64 v14, v14, v38, s[2:3]
	v_add_f32_dpp v15, v15, v15 quad_perm:[1,0,3,2] row_mask:0xf bank_mask:0xf bound_ctrl:1
	v_lshl_add_u32 v14, v14, 7, v20
	s_add_i32 s33, s31, 13
	v_add_f32_dpp v15, v15, v15 quad_perm:[2,3,0,1] row_mask:0xf bank_mask:0xf bound_ctrl:1
	s_nop 1
	v_add_f32_dpp v15, v15, v15 row_half_mirror row_mask:0xf bank_mask:0xf bound_ctrl:1
	s_nop 1
	v_add_f32_dpp v15, v15, v15 row_mirror row_mask:0xf bank_mask:0xf bound_ctrl:1
	v_mov_b32_e32 v21, v15
	s_nop 1
	v_permlane16_swap_b32_e32 v15, v21
	v_add_f32_e32 v15, v15, v21
	v_fmamk_f32 v15, v15, 0x3c000000, v186
	v_rsq_f32_e32 v21, v15
	ds_read_b64 v[14:15], v14
	v_mul_f32_e32 v16, v21, v16
	v_mul_f32_e32 v17, v21, v17
	v_mul_f32_e32 v18, v21, v18
	v_mul_f32_e32 v19, v21, v19
	v_mul_f32_e32 v16, v0, v16
	v_mul_f32_e32 v17, v1, v17
	v_mul_f32_e32 v18, v2, v18
	v_mul_f32_e32 v19, v3, v19
	s_waitcnt lgkmcnt(0)
	v_lshlrev_b32_e32 v21, 16, v14
	v_and_b32_e32 v14, 0xffff0000, v14
	v_lshlrev_b32_e32 v23, 16, v15
	v_and_b32_e32 v15, 0xffff0000, v15
	v_mul_f32_e32 v22, v18, v14
	v_mul_f32_e32 v24, v19, v15
	v_mul_f32_e32 v14, v16, v14
	v_mul_f32_e32 v15, v17, v15
	v_fma_f32 v22, v16, v21, -v22
	v_fmac_f32_e32 v14, v18, v21
	v_fmac_f32_e32 v15, v19, v23
	v_fma_f32 v24, v17, v23, -v24
	v_cvt_pk_bf16_f32 v22, v22, v24
	global_store_dword v[12:13], v22, off
	v_cvt_pk_bf16_f32 v14, v14, v15
	s_waitcnt vmcnt(14)
	v_and_b32_e32 v15, 0xffff0000, v32
	s_waitcnt vmcnt(13)
	v_and_b32_e32 v17, 0xffff0000, v33
	global_store_dword v[12:13], v14, off offset:64
	v_lshlrev_b32_e32 v14, 16, v32
	v_lshlrev_b32_e32 v16, 16, v33
	v_mul_f32_e32 v13, v15, v15
	v_mul_f32_e32 v18, v17, v17
	v_fmac_f32_e32 v13, v14, v14
	v_fmac_f32_e32 v18, v16, v16
	v_add_f32_e32 v13, v13, v18
	v_mov_b32_e32 v12, s33
	v_cndmask_b32_e64 v12, v12, v38, s[2:3]
	v_add_f32_dpp v13, v13, v13 quad_perm:[1,0,3,2] row_mask:0xf bank_mask:0xf bound_ctrl:1
	v_lshl_add_u32 v12, v12, 7, v20
	s_add_i32 s33, s31, 14
	v_add_f32_dpp v13, v13, v13 quad_perm:[2,3,0,1] row_mask:0xf bank_mask:0xf bound_ctrl:1
	s_add_i32 s31, s31, 15
	s_cmp_lt_u32 s30, 24
	v_add_f32_dpp v13, v13, v13 row_half_mirror row_mask:0xf bank_mask:0xf bound_ctrl:1
	s_nop 1
	v_add_f32_dpp v13, v13, v13 row_mirror row_mask:0xf bank_mask:0xf bound_ctrl:1
	v_mov_b32_e32 v18, v13
	s_nop 1
	v_permlane16_swap_b32_e32 v13, v18
	v_add_f32_e32 v13, v13, v18
	v_fmamk_f32 v13, v13, 0x3c000000, v186
	v_rsq_f32_e32 v18, v13
	ds_read_b64 v[12:13], v12
	v_mul_f32_e32 v14, v18, v14
	v_mul_f32_e32 v15, v18, v15
	v_mul_f32_e32 v16, v18, v16
	v_mul_f32_e32 v17, v18, v17
	v_mul_f32_e32 v14, v0, v14
	v_mul_f32_e32 v15, v1, v15
	v_mul_f32_e32 v16, v2, v16
	v_mul_f32_e32 v17, v3, v17
	s_waitcnt lgkmcnt(0)
	v_lshlrev_b32_e32 v18, 16, v12
	v_and_b32_e32 v12, 0xffff0000, v12
	v_lshlrev_b32_e32 v21, 16, v13
	v_and_b32_e32 v13, 0xffff0000, v13
	v_mul_f32_e32 v19, v16, v12
	v_mul_f32_e32 v22, v17, v13
	v_mul_f32_e32 v12, v14, v12
	v_mul_f32_e32 v13, v15, v13
	v_fma_f32 v19, v14, v18, -v19
	v_fmac_f32_e32 v12, v16, v18
	v_fmac_f32_e32 v13, v17, v21
	v_fma_f32 v22, v15, v21, -v22
	v_cvt_pk_bf16_f32 v19, v19, v22
	global_store_dword v[10:11], v19, off
	v_cvt_pk_bf16_f32 v12, v12, v13
	s_waitcnt vmcnt(14)
	v_and_b32_e32 v13, 0xffff0000, v34
	s_waitcnt vmcnt(13)
	v_and_b32_e32 v15, 0xffff0000, v35
	global_store_dword v[10:11], v12, off offset:64
	v_lshlrev_b32_e32 v12, 16, v34
	v_lshlrev_b32_e32 v14, 16, v35
	v_mul_f32_e32 v11, v13, v13
	v_mul_f32_e32 v16, v15, v15
	v_fmac_f32_e32 v11, v12, v12
	v_fmac_f32_e32 v16, v14, v14
	v_add_f32_e32 v11, v11, v16
	v_mov_b32_e32 v10, s33
	v_cndmask_b32_e64 v10, v10, v38, s[2:3]
	v_add_f32_dpp v11, v11, v11 quad_perm:[1,0,3,2] row_mask:0xf bank_mask:0xf bound_ctrl:1
	v_lshl_add_u32 v10, v10, 7, v20
	s_nop 0
	v_add_f32_dpp v11, v11, v11 quad_perm:[2,3,0,1] row_mask:0xf bank_mask:0xf bound_ctrl:1
	s_nop 1
	v_add_f32_dpp v11, v11, v11 row_half_mirror row_mask:0xf bank_mask:0xf bound_ctrl:1
	s_nop 1
	v_add_f32_dpp v11, v11, v11 row_mirror row_mask:0xf bank_mask:0xf bound_ctrl:1
	v_mov_b32_e32 v16, v11
	s_nop 1
	v_permlane16_swap_b32_e32 v11, v16
	v_add_f32_e32 v11, v11, v16
	v_fmamk_f32 v11, v11, 0x3c000000, v186
	v_rsq_f32_e32 v16, v11
	ds_read_b64 v[10:11], v10
	v_mul_f32_e32 v12, v16, v12
	v_mul_f32_e32 v13, v16, v13
	v_mul_f32_e32 v14, v16, v14
	v_mul_f32_e32 v15, v16, v15
	v_mul_f32_e32 v12, v0, v12
	v_mul_f32_e32 v13, v1, v13
	v_mul_f32_e32 v14, v2, v14
	v_mul_f32_e32 v15, v3, v15
	s_waitcnt lgkmcnt(0)
	v_lshlrev_b32_e32 v16, 16, v10
	v_and_b32_e32 v10, 0xffff0000, v10
	v_lshlrev_b32_e32 v18, 16, v11
	v_and_b32_e32 v11, 0xffff0000, v11
	v_mul_f32_e32 v17, v14, v10
	v_mul_f32_e32 v19, v15, v11
	v_mul_f32_e32 v10, v12, v10
	v_mul_f32_e32 v11, v13, v11
	v_fma_f32 v17, v12, v16, -v17
	v_fmac_f32_e32 v10, v14, v16
	v_fmac_f32_e32 v11, v15, v18
	v_fma_f32 v19, v13, v18, -v19
	v_cvt_pk_bf16_f32 v17, v17, v19
	global_store_dword v[8:9], v17, off
	v_cvt_pk_bf16_f32 v10, v10, v11
	s_waitcnt vmcnt(14)
	v_and_b32_e32 v11, 0xffff0000, v36
	s_waitcnt vmcnt(13)
	v_and_b32_e32 v13, 0xffff0000, v37
	global_store_dword v[8:9], v10, off offset:64
	v_lshlrev_b32_e32 v10, 16, v36
	v_lshlrev_b32_e32 v12, 16, v37
	v_mul_f32_e32 v9, v11, v11
	v_mul_f32_e32 v14, v13, v13
	v_fmac_f32_e32 v9, v10, v10
	v_fmac_f32_e32 v14, v12, v12
	v_add_f32_e32 v9, v9, v14
	v_mov_b32_e32 v8, s31
	v_cndmask_b32_e64 v8, v8, v38, s[2:3]
	v_add_f32_dpp v9, v9, v9 quad_perm:[1,0,3,2] row_mask:0xf bank_mask:0xf bound_ctrl:1
	v_lshl_add_u32 v8, v8, 7, v20
	s_nop 0
	v_add_f32_dpp v9, v9, v9 quad_perm:[2,3,0,1] row_mask:0xf bank_mask:0xf bound_ctrl:1
	s_nop 1
	v_add_f32_dpp v9, v9, v9 row_half_mirror row_mask:0xf bank_mask:0xf bound_ctrl:1
	s_nop 1
	v_add_f32_dpp v9, v9, v9 row_mirror row_mask:0xf bank_mask:0xf bound_ctrl:1
	v_mov_b32_e32 v14, v9
	s_nop 1
	v_permlane16_swap_b32_e32 v9, v14
	v_add_f32_e32 v9, v9, v14
	v_fmamk_f32 v9, v9, 0x3c000000, v186
	v_rsq_f32_e32 v14, v9
	ds_read_b64 v[8:9], v8
	v_mul_f32_e32 v10, v14, v10
	v_mul_f32_e32 v12, v14, v12
	v_mul_f32_e32 v10, v0, v10
	v_mul_f32_e32 v11, v14, v11
	v_mul_f32_e32 v12, v2, v12
	v_mul_f32_e32 v13, v14, v13
	s_waitcnt lgkmcnt(0)
	v_lshlrev_b32_e32 v14, 16, v8
	v_and_b32_e32 v8, 0xffff0000, v8
	v_mul_f32_e32 v11, v1, v11
	v_mul_f32_e32 v13, v3, v13
	v_mul_f32_e32 v15, v12, v8
	v_lshlrev_b32_e32 v16, 16, v9
	v_and_b32_e32 v9, 0xffff0000, v9
	v_mul_f32_e32 v8, v10, v8
	v_fma_f32 v15, v10, v14, -v15
	v_mul_f32_e32 v17, v13, v9
	v_fmac_f32_e32 v8, v12, v14
	v_mul_f32_e32 v9, v11, v9
	v_fma_f32 v17, v11, v16, -v17
	v_cvt_pk_bf16_f32 v15, v15, v17
	global_store_dword v[6:7], v15, off
	v_fmac_f32_e32 v9, v13, v16
	v_cvt_pk_bf16_f32 v8, v8, v9
	global_store_dword v[6:7], v8, off offset:64
	s_cbranch_scc1 .LBB0_1242

.LBB0_2065:
	s_and_b32 s0, s89, 0xffffffc0
	v_add_u32_e32 v0, s0, v144
	v_and_b32_e32 v112, 63, v144
	v_lshlrev_b32_e32 v1, 1, v0
	s_movk_i32 s2, 0xff80
	s_waitcnt vmcnt(0)
	s_waitcnt vmcnt(0)
	s_barrier
	s_waitcnt vmcnt(0)
	v_and_or_b32 v8, v1, s2, v112
	s_movk_i32 s0, 0x80
	s_add_u32 s4, s94, 0x402000
	v_ashrrev_i32_e32 v9, 31, v8
	v_cmp_gt_i32_e64 s[0:1], s0, v0
	s_addc_u32 s5, s95, 0
	v_and_b32_e32 v113, 0xffffffc0, v0
	v_cmp_gt_u32_e64 s[2:3], 64, v0
	v_lshl_add_u64 v[0:1], v[8:9], 2, s[6:7]
	s_mov_b32 s14, 0
	v_mov_b64_e32 v[2:3], 0x100
	v_mov_b64_e32 v[4:5], 0xff
	v_mov_b32_e32 v7, 0
	v_lshlrev_b64 v[8:9], 1, v[8:9]
	s_mov_b64 s[6:7], 0x46600200
	s_movk_i32 s15, 0x7fff
	s_mov_b32 s16, 0x46600000
	s_branch .LBB0_2068

.LBB0_2077:
	s_add_i32 s9, s18, 31
	v_mov_b32_e32 v6, s9
	v_mov_b32_e32 v16, s19
	v_cndmask_b32_e64 v6, v6, v16, s[2:3]
	v_lshl_add_u64 v[16:17], s[12:13], 0, v[6:7]
	v_lshlrev_b64 v[26:27], 10, v[16:17]
	v_lshl_add_u64 v[16:17], v[0:1], 0, v[26:27]
	s_add_i32 s9, s18, 30
	s_add_i32 s20, s19, 1
	global_load_dword v115, v[16:17], off sc1
	global_load_dword v114, v[16:17], off offset:256 sc1
	v_mov_b32_e32 v6, s9
	v_mov_b32_e32 v16, s20
	v_cndmask_b32_e64 v6, v6, v16, s[2:3]
	v_lshl_add_u64 v[16:17], s[12:13], 0, v[6:7]
	v_lshlrev_b64 v[18:19], 10, v[16:17]
	v_lshl_add_u64 v[20:21], v[0:1], 0, v[18:19]
	s_add_i32 s9, s18, 29
	s_add_i32 s20, s19, 2
	global_load_dword v16, v[20:21], off sc1
	global_load_dword v17, v[20:21], off offset:256 sc1
	v_mov_b32_e32 v6, s9
	v_mov_b32_e32 v20, s20
	v_cndmask_b32_e64 v6, v6, v20, s[2:3]
	v_lshl_add_u64 v[20:21], s[12:13], 0, v[6:7]
	v_lshlrev_b64 v[22:23], 10, v[20:21]
	v_lshl_add_u64 v[20:21], v[0:1], 0, v[22:23]
	s_add_i32 s9, s18, 28
	s_add_i32 s20, s19, 3
	global_load_dword v117, v[20:21], off sc1
	global_load_dword v116, v[20:21], off offset:256 sc1
	v_mov_b32_e32 v6, s9
	v_mov_b32_e32 v20, s20
	v_cndmask_b32_e64 v6, v6, v20, s[2:3]
	v_lshl_add_u64 v[20:21], s[12:13], 0, v[6:7]
	v_lshlrev_b64 v[24:25], 10, v[20:21]
	v_lshl_add_u64 v[28:29], v[0:1], 0, v[24:25]
	s_add_i32 s9, s18, 27
	s_add_i32 s20, s19, 4
	global_load_dword v20, v[28:29], off sc1
	global_load_dword v21, v[28:29], off offset:256 sc1
	v_mov_b32_e32 v6, s9
	v_mov_b32_e32 v28, s20
	v_cndmask_b32_e64 v6, v6, v28, s[2:3]
	v_lshl_add_u64 v[28:29], s[12:13], 0, v[6:7]
	v_lshlrev_b64 v[30:31], 10, v[28:29]
	v_lshl_add_u64 v[28:29], v[0:1], 0, v[30:31]
	s_add_i32 s9, s18, 26
	s_add_i32 s20, s19, 5
	global_load_dword v119, v[28:29], off sc1
	global_load_dword v118, v[28:29], off offset:256 sc1
	v_mov_b32_e32 v6, s9
	v_mov_b32_e32 v28, s20
	v_cndmask_b32_e64 v6, v6, v28, s[2:3]
	v_lshl_add_u64 v[28:29], s[12:13], 0, v[6:7]
	v_lshlrev_b64 v[32:33], 10, v[28:29]
	v_lshl_add_u64 v[34:35], v[0:1], 0, v[32:33]
	s_add_i32 s9, s18, 25
	s_add_i32 s20, s19, 6
	global_load_dword v28, v[34:35], off sc1
	global_load_dword v29, v[34:35], off offset:256 sc1
	v_mov_b32_e32 v6, s9
	v_mov_b32_e32 v34, s20
	v_cndmask_b32_e64 v6, v6, v34, s[2:3]
	v_lshl_add_u64 v[34:35], s[12:13], 0, v[6:7]
	v_lshlrev_b64 v[36:37], 10, v[34:35]
	v_lshl_add_u64 v[34:35], v[0:1], 0, v[36:37]
	s_add_i32 s9, s18, 24
	s_add_i32 s20, s19, 7
	global_load_dword v121, v[34:35], off sc1
	global_load_dword v120, v[34:35], off offset:256 sc1
	v_mov_b32_e32 v6, s9
	v_mov_b32_e32 v34, s20
	v_cndmask_b32_e64 v6, v6, v34, s[2:3]
	v_lshl_add_u64 v[34:35], s[12:13], 0, v[6:7]
	v_lshlrev_b64 v[38:39], 10, v[34:35]
	v_lshl_add_u64 v[40:41], v[0:1], 0, v[38:39]
	s_add_i32 s9, s18, 23
	s_add_i32 s20, s19, 8
	global_load_dword v34, v[40:41], off sc1
	global_load_dword v35, v[40:41], off offset:256 sc1
	v_mov_b32_e32 v6, s9
	v_mov_b32_e32 v40, s20
	v_cndmask_b32_e64 v6, v6, v40, s[2:3]
	v_lshl_add_u64 v[40:41], s[12:13], 0, v[6:7]
	v_lshlrev_b64 v[42:43], 10, v[40:41]
	v_lshl_add_u64 v[40:41], v[0:1], 0, v[42:43]
	s_add_i32 s9, s18, 22
	s_add_i32 s20, s19, 9
	global_load_dword v123, v[40:41], off sc1
	global_load_dword v122, v[40:41], off offset:256 sc1
	v_mov_b32_e32 v6, s9
	v_mov_b32_e32 v40, s20
	v_cndmask_b32_e64 v6, v6, v40, s[2:3]
	v_lshl_add_u64 v[40:41], s[12:13], 0, v[6:7]
	v_lshlrev_b64 v[44:45], 10, v[40:41]
	v_lshl_add_u64 v[46:47], v[0:1], 0, v[44:45]
	s_add_i32 s9, s18, 21
	s_add_i32 s20, s19, 10
	global_load_dword v40, v[46:47], off sc1
	global_load_dword v41, v[46:47], off offset:256 sc1
	v_mov_b32_e32 v6, s9
	v_mov_b32_e32 v46, s20
	v_cndmask_b32_e64 v6, v6, v46, s[2:3]
	v_lshl_add_u64 v[46:47], s[12:13], 0, v[6:7]
	v_lshlrev_b64 v[48:49], 10, v[46:47]
	v_lshl_add_u64 v[46:47], v[0:1], 0, v[48:49]
	s_add_i32 s9, s18, 20
	s_add_i32 s20, s19, 11
	global_load_dword v125, v[46:47], off sc1
	global_load_dword v124, v[46:47], off offset:256 sc1
	v_mov_b32_e32 v6, s9
	v_mov_b32_e32 v46, s20
	v_cndmask_b32_e64 v6, v6, v46, s[2:3]
	v_lshl_add_u64 v[46:47], s[12:13], 0, v[6:7]
	v_lshlrev_b64 v[50:51], 10, v[46:47]
	v_lshl_add_u64 v[52:53], v[0:1], 0, v[50:51]
	s_add_i32 s9, s18, 19
	s_add_i32 s20, s19, 12
	global_load_dword v46, v[52:53], off sc1
	global_load_dword v47, v[52:53], off offset:256 sc1
	v_mov_b32_e32 v6, s9
	v_mov_b32_e32 v52, s20
	v_cndmask_b32_e64 v6, v6, v52, s[2:3]
	v_lshl_add_u64 v[52:53], s[12:13], 0, v[6:7]
	v_lshlrev_b64 v[54:55], 10, v[52:53]
	v_lshl_add_u64 v[52:53], v[0:1], 0, v[54:55]
	s_add_i32 s9, s18, 18
	s_add_i32 s20, s19, 13
	global_load_dword v127, v[52:53], off sc1
	global_load_dword v126, v[52:53], off offset:256 sc1
	v_mov_b32_e32 v6, s9
	v_mov_b32_e32 v52, s20
	v_cndmask_b32_e64 v6, v6, v52, s[2:3]
	v_lshl_add_u64 v[52:53], s[12:13], 0, v[6:7]
	v_lshlrev_b64 v[56:57], 10, v[52:53]
	v_lshl_add_u64 v[58:59], v[0:1], 0, v[56:57]
	s_add_i32 s9, s18, 17
	s_add_i32 s20, s19, 14
	global_load_dword v52, v[58:59], off sc1
	global_load_dword v53, v[58:59], off offset:256 sc1
	v_mov_b32_e32 v6, s9
	v_mov_b32_e32 v58, s20
	v_cndmask_b32_e64 v6, v6, v58, s[2:3]
	v_lshl_add_u64 v[58:59], s[12:13], 0, v[6:7]
	v_lshlrev_b64 v[60:61], 10, v[58:59]
	v_lshl_add_u64 v[58:59], v[0:1], 0, v[60:61]
	s_add_i32 s9, s18, 16
	s_add_i32 s20, s19, 15
	global_load_dword v129, v[58:59], off sc1
	global_load_dword v128, v[58:59], off offset:256 sc1
	v_mov_b32_e32 v6, s9
	v_mov_b32_e32 v58, s20
	v_cndmask_b32_e64 v6, v6, v58, s[2:3]
	v_lshl_add_u64 v[58:59], s[12:13], 0, v[6:7]
	v_lshlrev_b64 v[62:63], 10, v[58:59]
	v_lshl_add_u64 v[64:65], v[0:1], 0, v[62:63]
	s_add_i32 s9, s18, 15
	s_add_i32 s20, s19, 16
	global_load_dword v58, v[64:65], off sc1
	global_load_dword v59, v[64:65], off offset:256 sc1
	v_mov_b32_e32 v6, s9
	v_mov_b32_e32 v64, s20
	v_cndmask_b32_e64 v6, v6, v64, s[2:3]
	v_lshl_add_u64 v[64:65], s[12:13], 0, v[6:7]
	v_lshlrev_b64 v[66:67], 10, v[64:65]
	v_lshl_add_u64 v[64:65], v[0:1], 0, v[66:67]
	s_add_i32 s9, s18, 14
	s_add_i32 s20, s19, 17
	global_load_dword v131, v[64:65], off sc1
	global_load_dword v130, v[64:65], off offset:256 sc1
	v_mov_b32_e32 v6, s9
	v_mov_b32_e32 v64, s20
	v_cndmask_b32_e64 v6, v6, v64, s[2:3]
	v_lshl_add_u64 v[64:65], s[12:13], 0, v[6:7]
	v_lshlrev_b64 v[68:69], 10, v[64:65]
	v_lshl_add_u64 v[70:71], v[0:1], 0, v[68:69]
	s_add_i32 s9, s18, 13
	s_add_i32 s20, s19, 18
	global_load_dword v64, v[70:71], off sc1
	global_load_dword v65, v[70:71], off offset:256 sc1
	v_mov_b32_e32 v6, s9
	v_mov_b32_e32 v70, s20
	v_cndmask_b32_e64 v6, v6, v70, s[2:3]
	v_lshl_add_u64 v[70:71], s[12:13], 0, v[6:7]
	v_lshlrev_b64 v[72:73], 10, v[70:71]
	v_lshl_add_u64 v[70:71], v[0:1], 0, v[72:73]
	s_add_i32 s9, s18, 12
	s_add_i32 s20, s19, 19
	global_load_dword v133, v[70:71], off sc1
	global_load_dword v132, v[70:71], off offset:256 sc1
	v_mov_b32_e32 v6, s9
	v_mov_b32_e32 v70, s20
	v_cndmask_b32_e64 v6, v6, v70, s[2:3]
	v_lshl_add_u64 v[70:71], s[12:13], 0, v[6:7]
	v_lshlrev_b64 v[74:75], 10, v[70:71]
	v_lshl_add_u64 v[76:77], v[0:1], 0, v[74:75]
	s_add_i32 s9, s18, 11
	s_add_i32 s20, s19, 20
	global_load_dword v70, v[76:77], off sc1
	global_load_dword v71, v[76:77], off offset:256 sc1
	v_mov_b32_e32 v6, s9
	v_mov_b32_e32 v76, s20
	v_cndmask_b32_e64 v6, v6, v76, s[2:3]
	v_lshl_add_u64 v[76:77], s[12:13], 0, v[6:7]
	v_lshlrev_b64 v[78:79], 10, v[76:77]
	v_lshl_add_u64 v[76:77], v[0:1], 0, v[78:79]
	s_add_i32 s9, s18, 10
	s_add_i32 s20, s19, 21
	global_load_dword v135, v[76:77], off sc1
	global_load_dword v134, v[76:77], off offset:256 sc1
	v_mov_b32_e32 v6, s9
	v_mov_b32_e32 v76, s20
	v_cndmask_b32_e64 v6, v6, v76, s[2:3]
	v_lshl_add_u64 v[76:77], s[12:13], 0, v[6:7]
	v_lshlrev_b64 v[80:81], 10, v[76:77]
	v_lshl_add_u64 v[82:83], v[0:1], 0, v[80:81]
	s_add_i32 s9, s18, 9
	s_add_i32 s20, s19, 22
	global_load_dword v76, v[82:83], off sc1
	global_load_dword v77, v[82:83], off offset:256 sc1
	v_mov_b32_e32 v6, s9
	v_mov_b32_e32 v82, s20
	v_cndmask_b32_e64 v6, v6, v82, s[2:3]
	v_lshl_add_u64 v[82:83], s[12:13], 0, v[6:7]
	v_lshlrev_b64 v[84:85], 10, v[82:83]
	v_lshl_add_u64 v[82:83], v[0:1], 0, v[84:85]
	s_add_i32 s9, s18, 8
	s_add_i32 s20, s19, 23
	global_load_dword v137, v[82:83], off sc1
	global_load_dword v136, v[82:83], off offset:256 sc1
	v_mov_b32_e32 v6, s9
	v_mov_b32_e32 v82, s20
	v_cndmask_b32_e64 v6, v6, v82, s[2:3]
	v_lshl_add_u64 v[82:83], s[12:13], 0, v[6:7]
	v_lshlrev_b64 v[86:87], 10, v[82:83]
	v_lshl_add_u64 v[88:89], v[0:1], 0, v[86:87]
	s_add_i32 s9, s18, 7
	s_add_i32 s20, s19, 24
	global_load_dword v82, v[88:89], off sc1
	global_load_dword v83, v[88:89], off offset:256 sc1
	v_mov_b32_e32 v6, s9
	v_mov_b32_e32 v88, s20
	v_cndmask_b32_e64 v6, v6, v88, s[2:3]
	v_lshl_add_u64 v[88:89], s[12:13], 0, v[6:7]
	v_lshlrev_b64 v[90:91], 10, v[88:89]
	v_lshl_add_u64 v[88:89], v[0:1], 0, v[90:91]
	s_add_i32 s9, s18, 6
	s_add_i32 s20, s19, 25
	global_load_dword v139, v[88:89], off sc1
	global_load_dword v138, v[88:89], off offset:256 sc1
	v_mov_b32_e32 v6, s9
	v_mov_b32_e32 v88, s20
	v_cndmask_b32_e64 v6, v6, v88, s[2:3]
	v_lshl_add_u64 v[88:89], s[12:13], 0, v[6:7]
	v_lshlrev_b64 v[92:93], 10, v[88:89]
	v_lshl_add_u64 v[94:95], v[0:1], 0, v[92:93]
	s_add_i32 s9, s18, 5
	s_add_i32 s20, s19, 26
	global_load_dword v88, v[94:95], off sc1
	global_load_dword v89, v[94:95], off offset:256 sc1
	v_mov_b32_e32 v6, s9
	v_mov_b32_e32 v94, s20
	v_cndmask_b32_e64 v6, v6, v94, s[2:3]
	v_lshl_add_u64 v[94:95], s[12:13], 0, v[6:7]
	v_lshlrev_b64 v[96:97], 10, v[94:95]
	v_lshl_add_u64 v[94:95], v[0:1], 0, v[96:97]
	s_add_i32 s9, s18, 4
	s_add_i32 s20, s19, 27
	global_load_dword v141, v[94:95], off sc1
	global_load_dword v140, v[94:95], off offset:256 sc1
	v_mov_b32_e32 v6, s9
	v_mov_b32_e32 v94, s20
	v_cndmask_b32_e64 v6, v6, v94, s[2:3]
	v_lshl_add_u64 v[94:95], s[12:13], 0, v[6:7]
	v_lshlrev_b64 v[98:99], 10, v[94:95]
	v_lshl_add_u64 v[100:101], v[0:1], 0, v[98:99]
	s_add_i32 s9, s18, 3
	s_add_i32 s20, s19, 28
	global_load_dword v94, v[100:101], off sc1
	global_load_dword v95, v[100:101], off offset:256 sc1
	v_mov_b32_e32 v6, s9
	v_mov_b32_e32 v100, s20
	v_cndmask_b32_e64 v6, v6, v100, s[2:3]
	v_lshl_add_u64 v[100:101], s[12:13], 0, v[6:7]
	v_lshlrev_b64 v[102:103], 10, v[100:101]
	v_lshl_add_u64 v[100:101], v[0:1], 0, v[102:103]
	s_add_i32 s9, s18, 2
	s_add_i32 s20, s19, 29
	global_load_dword v143, v[100:101], off sc1
	global_load_dword v142, v[100:101], off offset:256 sc1
	v_mov_b32_e32 v6, s9
	v_mov_b32_e32 v100, s20
	v_cndmask_b32_e64 v6, v6, v100, s[2:3]
	v_lshl_add_u64 v[100:101], s[12:13], 0, v[6:7]
	v_lshlrev_b64 v[104:105], 10, v[100:101]
	v_lshl_add_u64 v[106:107], v[0:1], 0, v[104:105]
	s_add_i32 s9, s18, 1
	s_add_i32 s20, s19, 30
	global_load_dword v100, v[106:107], off sc1
	global_load_dword v101, v[106:107], off offset:256 sc1
	v_mov_b32_e32 v6, s9
	v_mov_b32_e32 v106, s20
	v_cndmask_b32_e64 v6, v6, v106, s[2:3]
	v_lshl_add_u64 v[106:107], s[12:13], 0, v[6:7]
	v_lshlrev_b64 v[106:107], 10, v[106:107]
	v_lshl_add_u64 v[108:109], v[0:1], 0, v[106:107]
	s_add_i32 s9, s19, 31
	global_load_dword v145, v[108:109], off sc1
	global_load_dword v144, v[108:109], off offset:256 sc1
	v_mov_b32_e32 v6, s18
	v_mov_b32_e32 v108, s9
	v_cndmask_b32_e64 v6, v6, v108, s[2:3]
	v_lshl_add_u64 v[108:109], s[12:13], 0, v[6:7]
	v_lshlrev_b64 v[110:111], 10, v[108:109]
	v_lshl_add_u64 v[26:27], s[94:95], 0, v[26:27]
	v_lshl_add_u64 v[146:147], v[0:1], 0, v[110:111]
	v_lshl_add_u64 v[26:27], v[26:27], 0, v[8:9]
	global_load_dword v108, v[146:147], off sc1
	global_load_dword v109, v[146:147], off offset:256 sc1
	v_lshl_add_u64 v[146:147], v[26:27], 0, s[6:7]
	v_bfe_u32 v6, v14, 16, 1
	v_add_co_u32_e32 v26, vcc, s16, v26
	v_add3_u32 v6, v14, v6, s15
	s_nop 0
	v_addc_co_u32_e32 v27, vcc, 0, v27, vcc
	global_store_short_d16_hi v[26:27], v6, off offset:512
	v_bfe_u32 v6, v15, 16, 1
	v_add3_u32 v6, v15, v6, s15
	v_pk_mul_f32 v[26:27], v[10:11], v[14:15]
	global_store_short_d16_hi v[146:147], v6, off offset:128
	v_sub_f32_e32 v6, v26, v27
	v_lshl_add_u64 v[18:19], s[94:95], 0, v[18:19]
	s_waitcnt vmcnt(62)
	v_add_f32_e32 v6, v115, v6
	v_pk_mul_f32 v[14:15], v[12:13], v[14:15]
	v_lshl_add_u64 v[18:19], v[18:19], 0, v[8:9]
	v_add_f32_e32 v14, v14, v15
	v_lshl_add_u64 v[26:27], v[18:19], 0, s[6:7]
	v_bfe_u32 v15, v6, 16, 1
	v_add_co_u32_e32 v18, vcc, s16, v18
	v_add_f32_e32 v14, v14, v114
	v_add3_u32 v15, v6, v15, s15
	v_addc_co_u32_e32 v19, vcc, 0, v19, vcc
	global_store_short_d16_hi v[18:19], v15, off offset:512
	v_bfe_u32 v15, v14, 16, 1
	v_add3_u32 v15, v14, v15, s15
	global_store_short_d16_hi v[26:27], v15, off offset:128
	v_pk_mul_f32 v[14:15], v[12:13], v[14:15] op_sel_hi:[1,0]
	v_lshl_add_u64 v[18:19], s[94:95], 0, v[22:23]
	v_pk_fma_f32 v[26:27], v[10:11], v[6:7], v[14:15] neg_lo:[0,0,1] neg_hi:[0,0,1]
	v_pk_fma_f32 v[14:15], v[10:11], v[6:7], v[14:15] op_sel_hi:[1,0,1]
	v_lshl_add_u64 v[18:19], v[18:19], 0, v[8:9]
	v_mov_b32_e32 v27, v15
	v_pk_add_f32 v[14:15], v[16:17], v[26:27]
	v_add_co_u32_e32 v16, vcc, s16, v18
	v_bfe_u32 v6, v14, 16, 1
	v_add3_u32 v6, v14, v6, s15
	v_addc_co_u32_e32 v17, vcc, 0, v19, vcc
	global_store_short_d16_hi v[16:17], v6, off offset:512
	v_bfe_u32 v6, v15, 16, 1
	v_lshl_add_u64 v[22:23], v[18:19], 0, s[6:7]
	v_add3_u32 v6, v15, v6, s15
	v_pk_mul_f32 v[16:17], v[10:11], v[14:15]
	global_store_short_d16_hi v[22:23], v6, off offset:128
	v_sub_f32_e32 v6, v16, v17
	v_lshl_add_u64 v[16:17], s[94:95], 0, v[24:25]
	s_waitcnt vmcnt(62)
	v_add_f32_e32 v6, v117, v6
	v_pk_mul_f32 v[14:15], v[10:11], v[14:15] op_sel:[0,1] op_sel_hi:[1,0]
	v_lshl_add_u64 v[16:17], v[16:17], 0, v[8:9]
	v_add_f32_e32 v14, v14, v15
	v_lshl_add_u64 v[18:19], v[16:17], 0, s[6:7]
	v_bfe_u32 v15, v6, 16, 1
	v_add_co_u32_e32 v16, vcc, s16, v16
	v_add_f32_e32 v14, v116, v14
	v_add3_u32 v15, v6, v15, s15
	v_addc_co_u32_e32 v17, vcc, 0, v17, vcc
	global_store_short_d16_hi v[16:17], v15, off offset:512
	v_bfe_u32 v15, v14, 16, 1
	v_add3_u32 v15, v14, v15, s15
	global_store_short_d16_hi v[18:19], v15, off offset:128
	v_pk_mul_f32 v[14:15], v[12:13], v[14:15] op_sel_hi:[1,0]
	v_lshl_add_u64 v[16:17], s[94:95], 0, v[30:31]
	v_pk_fma_f32 v[22:23], v[10:11], v[6:7], v[14:15] neg_lo:[0,0,1] neg_hi:[0,0,1]
	v_pk_fma_f32 v[14:15], v[10:11], v[6:7], v[14:15] op_sel_hi:[1,0,1]
	v_lshl_add_u64 v[16:17], v[16:17], 0, v[8:9]
	v_mov_b32_e32 v23, v15
	v_pk_add_f32 v[14:15], v[20:21], v[22:23]
	v_lshl_add_u64 v[18:19], v[16:17], 0, s[6:7]
	v_bfe_u32 v6, v14, 16, 1
	v_add_co_u32_e32 v16, vcc, s16, v16
	v_add3_u32 v6, v14, v6, s15
	s_nop 0
	v_addc_co_u32_e32 v17, vcc, 0, v17, vcc
	global_store_short_d16_hi v[16:17], v6, off offset:512
	v_bfe_u32 v6, v15, 16, 1
	v_add3_u32 v6, v15, v6, s15
	v_pk_mul_f32 v[16:17], v[10:11], v[14:15]
	global_store_short_d16_hi v[18:19], v6, off offset:128
	v_sub_f32_e32 v6, v16, v17
	v_lshl_add_u64 v[16:17], s[94:95], 0, v[32:33]
	s_waitcnt vmcnt(62)
	v_add_f32_e32 v6, v119, v6
	v_pk_mul_f32 v[14:15], v[10:11], v[14:15] op_sel:[0,1] op_sel_hi:[1,0]
	v_lshl_add_u64 v[16:17], v[16:17], 0, v[8:9]
	v_add_f32_e32 v14, v14, v15
	v_lshl_add_u64 v[18:19], v[16:17], 0, s[6:7]
	v_bfe_u32 v15, v6, 16, 1
	v_add_co_u32_e32 v16, vcc, s16, v16
	v_add_f32_e32 v14, v118, v14
	v_add3_u32 v15, v6, v15, s15
	v_addc_co_u32_e32 v17, vcc, 0, v17, vcc
	global_store_short_d16_hi v[16:17], v15, off offset:512
	v_bfe_u32 v15, v14, 16, 1
	v_add3_u32 v15, v14, v15, s15
	global_store_short_d16_hi v[18:19], v15, off offset:128
	v_pk_mul_f32 v[14:15], v[12:13], v[14:15] op_sel_hi:[1,0]
	v_lshl_add_u64 v[16:17], s[94:95], 0, v[36:37]
	v_pk_fma_f32 v[20:21], v[10:11], v[6:7], v[14:15] neg_lo:[0,0,1] neg_hi:[0,0,1]
	v_pk_fma_f32 v[14:15], v[10:11], v[6:7], v[14:15] op_sel_hi:[1,0,1]
	v_lshl_add_u64 v[16:17], v[16:17], 0, v[8:9]
	v_mov_b32_e32 v21, v15
	v_pk_add_f32 v[14:15], v[28:29], v[20:21]
	v_lshl_add_u64 v[18:19], v[16:17], 0, s[6:7]
	v_bfe_u32 v6, v14, 16, 1
	v_add_co_u32_e32 v16, vcc, s16, v16
	v_add3_u32 v6, v14, v6, s15
	s_nop 0
	v_addc_co_u32_e32 v17, vcc, 0, v17, vcc
	global_store_short_d16_hi v[16:17], v6, off offset:512
	v_bfe_u32 v6, v15, 16, 1
	v_add3_u32 v6, v15, v6, s15
	v_pk_mul_f32 v[16:17], v[10:11], v[14:15]
	global_store_short_d16_hi v[18:19], v6, off offset:128
	v_sub_f32_e32 v6, v16, v17
	v_lshl_add_u64 v[16:17], s[94:95], 0, v[38:39]
	s_waitcnt vmcnt(62)
	v_add_f32_e32 v6, v121, v6
	v_pk_mul_f32 v[14:15], v[10:11], v[14:15] op_sel:[0,1] op_sel_hi:[1,0]
	v_lshl_add_u64 v[16:17], v[16:17], 0, v[8:9]
	v_add_f32_e32 v14, v14, v15
	v_lshl_add_u64 v[18:19], v[16:17], 0, s[6:7]
	v_bfe_u32 v15, v6, 16, 1
	v_add_co_u32_e32 v16, vcc, s16, v16
	v_add_f32_e32 v14, v120, v14
	v_add3_u32 v15, v6, v15, s15
	v_addc_co_u32_e32 v17, vcc, 0, v17, vcc
	global_store_short_d16_hi v[16:17], v15, off offset:512
	v_bfe_u32 v15, v14, 16, 1
	v_add3_u32 v15, v14, v15, s15
	global_store_short_d16_hi v[18:19], v15, off offset:128
	v_pk_mul_f32 v[14:15], v[12:13], v[14:15] op_sel_hi:[1,0]
	v_lshl_add_u64 v[16:17], s[94:95], 0, v[42:43]
	v_pk_fma_f32 v[20:21], v[10:11], v[6:7], v[14:15] neg_lo:[0,0,1] neg_hi:[0,0,1]
	v_pk_fma_f32 v[14:15], v[10:11], v[6:7], v[14:15] op_sel_hi:[1,0,1]
	v_lshl_add_u64 v[16:17], v[16:17], 0, v[8:9]
	v_mov_b32_e32 v21, v15
	v_pk_add_f32 v[14:15], v[34:35], v[20:21]
	v_lshl_add_u64 v[18:19], v[16:17], 0, s[6:7]
	v_bfe_u32 v6, v14, 16, 1
	v_add_co_u32_e32 v16, vcc, s16, v16
	v_add3_u32 v6, v14, v6, s15
	s_nop 0
	v_addc_co_u32_e32 v17, vcc, 0, v17, vcc
	global_store_short_d16_hi v[16:17], v6, off offset:512
	v_bfe_u32 v6, v15, 16, 1
	v_add3_u32 v6, v15, v6, s15
	v_pk_mul_f32 v[16:17], v[10:11], v[14:15]
	global_store_short_d16_hi v[18:19], v6, off offset:128
	v_sub_f32_e32 v6, v16, v17
	v_lshl_add_u64 v[16:17], s[94:95], 0, v[44:45]
	s_waitcnt vmcnt(62)
	v_add_f32_e32 v6, v123, v6
	v_pk_mul_f32 v[14:15], v[10:11], v[14:15] op_sel:[0,1] op_sel_hi:[1,0]
	v_lshl_add_u64 v[16:17], v[16:17], 0, v[8:9]
	v_add_f32_e32 v14, v14, v15
	v_lshl_add_u64 v[18:19], v[16:17], 0, s[6:7]
	v_bfe_u32 v15, v6, 16, 1
	v_add_co_u32_e32 v16, vcc, s16, v16
	v_add_f32_e32 v14, v122, v14
	v_add3_u32 v15, v6, v15, s15
	v_addc_co_u32_e32 v17, vcc, 0, v17, vcc
	global_store_short_d16_hi v[16:17], v15, off offset:512
	v_bfe_u32 v15, v14, 16, 1
	v_add3_u32 v15, v14, v15, s15
	global_store_short_d16_hi v[18:19], v15, off offset:128
	v_pk_mul_f32 v[14:15], v[12:13], v[14:15] op_sel_hi:[1,0]
	v_lshl_add_u64 v[16:17], s[94:95], 0, v[48:49]
	v_pk_fma_f32 v[20:21], v[10:11], v[6:7], v[14:15] neg_lo:[0,0,1] neg_hi:[0,0,1]
	v_pk_fma_f32 v[14:15], v[10:11], v[6:7], v[14:15] op_sel_hi:[1,0,1]
	v_lshl_add_u64 v[16:17], v[16:17], 0, v[8:9]
	v_mov_b32_e32 v21, v15
	v_pk_add_f32 v[14:15], v[40:41], v[20:21]
	v_lshl_add_u64 v[18:19], v[16:17], 0, s[6:7]
	v_bfe_u32 v6, v14, 16, 1
	v_add_co_u32_e32 v16, vcc, s16, v16
	v_add3_u32 v6, v14, v6, s15
	s_nop 0
	v_addc_co_u32_e32 v17, vcc, 0, v17, vcc
	global_store_short_d16_hi v[16:17], v6, off offset:512
	v_bfe_u32 v6, v15, 16, 1
	v_add3_u32 v6, v15, v6, s15
	v_pk_mul_f32 v[16:17], v[10:11], v[14:15]
	global_store_short_d16_hi v[18:19], v6, off offset:128
	v_sub_f32_e32 v6, v16, v17
	v_lshl_add_u64 v[16:17], s[94:95], 0, v[50:51]
	s_waitcnt vmcnt(62)
	v_add_f32_e32 v6, v125, v6
	v_pk_mul_f32 v[14:15], v[10:11], v[14:15] op_sel:[0,1] op_sel_hi:[1,0]
	v_lshl_add_u64 v[16:17], v[16:17], 0, v[8:9]
	v_add_f32_e32 v14, v14, v15
	v_lshl_add_u64 v[18:19], v[16:17], 0, s[6:7]
	v_bfe_u32 v15, v6, 16, 1
	v_add_co_u32_e32 v16, vcc, s16, v16
	v_add_f32_e32 v14, v124, v14
	v_add3_u32 v15, v6, v15, s15
	v_addc_co_u32_e32 v17, vcc, 0, v17, vcc
	global_store_short_d16_hi v[16:17], v15, off offset:512
	v_bfe_u32 v15, v14, 16, 1
	v_add3_u32 v15, v14, v15, s15
	global_store_short_d16_hi v[18:19], v15, off offset:128
	v_pk_mul_f32 v[14:15], v[12:13], v[14:15] op_sel_hi:[1,0]
	v_lshl_add_u64 v[16:17], s[94:95], 0, v[54:55]
	v_pk_fma_f32 v[20:21], v[10:11], v[6:7], v[14:15] neg_lo:[0,0,1] neg_hi:[0,0,1]
	v_pk_fma_f32 v[14:15], v[10:11], v[6:7], v[14:15] op_sel_hi:[1,0,1]
	v_lshl_add_u64 v[16:17], v[16:17], 0, v[8:9]
	v_mov_b32_e32 v21, v15
	v_pk_add_f32 v[14:15], v[46:47], v[20:21]
	v_lshl_add_u64 v[18:19], v[16:17], 0, s[6:7]
	v_bfe_u32 v6, v14, 16, 1
	v_add_co_u32_e32 v16, vcc, s16, v16
	v_add3_u32 v6, v14, v6, s15
	s_nop 0
	v_addc_co_u32_e32 v17, vcc, 0, v17, vcc
	global_store_short_d16_hi v[16:17], v6, off offset:512
	v_bfe_u32 v6, v15, 16, 1
	v_add3_u32 v6, v15, v6, s15
	v_pk_mul_f32 v[16:17], v[10:11], v[14:15]
	global_store_short_d16_hi v[18:19], v6, off offset:128
	v_sub_f32_e32 v6, v16, v17
	v_lshl_add_u64 v[16:17], s[94:95], 0, v[56:57]
	s_waitcnt vmcnt(62)
	v_add_f32_e32 v6, v127, v6
	v_pk_mul_f32 v[14:15], v[10:11], v[14:15] op_sel:[0,1] op_sel_hi:[1,0]
	v_lshl_add_u64 v[16:17], v[16:17], 0, v[8:9]
	v_add_f32_e32 v14, v14, v15
	v_lshl_add_u64 v[18:19], v[16:17], 0, s[6:7]
	v_bfe_u32 v15, v6, 16, 1
	v_add_co_u32_e32 v16, vcc, s16, v16
	v_add_f32_e32 v14, v126, v14
	v_add3_u32 v15, v6, v15, s15
	v_addc_co_u32_e32 v17, vcc, 0, v17, vcc
	global_store_short_d16_hi v[16:17], v15, off offset:512
	v_bfe_u32 v15, v14, 16, 1
	v_add3_u32 v15, v14, v15, s15
	global_store_short_d16_hi v[18:19], v15, off offset:128
	v_pk_mul_f32 v[14:15], v[12:13], v[14:15] op_sel_hi:[1,0]
	v_lshl_add_u64 v[16:17], s[94:95], 0, v[60:61]
	v_pk_fma_f32 v[20:21], v[10:11], v[6:7], v[14:15] neg_lo:[0,0,1] neg_hi:[0,0,1]
	v_pk_fma_f32 v[14:15], v[10:11], v[6:7], v[14:15] op_sel_hi:[1,0,1]
	v_lshl_add_u64 v[16:17], v[16:17], 0, v[8:9]
	v_mov_b32_e32 v21, v15
	v_pk_add_f32 v[14:15], v[52:53], v[20:21]
	v_lshl_add_u64 v[18:19], v[16:17], 0, s[6:7]
	v_bfe_u32 v6, v14, 16, 1
	v_add_co_u32_e32 v16, vcc, s16, v16
	v_add3_u32 v6, v14, v6, s15
	s_nop 0
	v_addc_co_u32_e32 v17, vcc, 0, v17, vcc
	global_store_short_d16_hi v[16:17], v6, off offset:512
	v_bfe_u32 v6, v15, 16, 1
	v_add3_u32 v6, v15, v6, s15
	v_pk_mul_f32 v[16:17], v[10:11], v[14:15]
	global_store_short_d16_hi v[18:19], v6, off offset:128
	v_sub_f32_e32 v6, v16, v17
	v_lshl_add_u64 v[16:17], s[94:95], 0, v[62:63]
	s_waitcnt vmcnt(62)
	v_add_f32_e32 v6, v129, v6
	v_pk_mul_f32 v[14:15], v[10:11], v[14:15] op_sel:[0,1] op_sel_hi:[1,0]
	v_lshl_add_u64 v[16:17], v[16:17], 0, v[8:9]
	v_add_f32_e32 v14, v14, v15
	v_lshl_add_u64 v[18:19], v[16:17], 0, s[6:7]
	v_bfe_u32 v15, v6, 16, 1
	v_add_co_u32_e32 v16, vcc, s16, v16
	v_add_f32_e32 v14, v128, v14
	v_add3_u32 v15, v6, v15, s15
	v_addc_co_u32_e32 v17, vcc, 0, v17, vcc
	global_store_short_d16_hi v[16:17], v15, off offset:512
	v_bfe_u32 v15, v14, 16, 1
	v_add3_u32 v15, v14, v15, s15
	global_store_short_d16_hi v[18:19], v15, off offset:128
	v_pk_mul_f32 v[14:15], v[12:13], v[14:15] op_sel_hi:[1,0]
	v_lshl_add_u64 v[16:17], s[94:95], 0, v[66:67]
	v_pk_fma_f32 v[20:21], v[10:11], v[6:7], v[14:15] neg_lo:[0,0,1] neg_hi:[0,0,1]
	v_pk_fma_f32 v[14:15], v[10:11], v[6:7], v[14:15] op_sel_hi:[1,0,1]
	v_lshl_add_u64 v[16:17], v[16:17], 0, v[8:9]
	v_mov_b32_e32 v21, v15
	v_pk_add_f32 v[14:15], v[58:59], v[20:21]
	v_lshl_add_u64 v[18:19], v[16:17], 0, s[6:7]
	v_bfe_u32 v6, v14, 16, 1
	v_add_co_u32_e32 v16, vcc, s16, v16
	v_add3_u32 v6, v14, v6, s15
	s_nop 0
	v_addc_co_u32_e32 v17, vcc, 0, v17, vcc
	global_store_short_d16_hi v[16:17], v6, off offset:512
	v_bfe_u32 v6, v15, 16, 1
	v_add3_u32 v6, v15, v6, s15
	v_pk_mul_f32 v[16:17], v[10:11], v[14:15]
	global_store_short_d16_hi v[18:19], v6, off offset:128
	v_sub_f32_e32 v6, v16, v17
	v_lshl_add_u64 v[16:17], s[94:95], 0, v[68:69]
	s_waitcnt vmcnt(62)
	v_add_f32_e32 v6, v131, v6
	v_pk_mul_f32 v[14:15], v[10:11], v[14:15] op_sel:[0,1] op_sel_hi:[1,0]
	v_lshl_add_u64 v[16:17], v[16:17], 0, v[8:9]
	v_add_f32_e32 v14, v14, v15
	v_lshl_add_u64 v[18:19], v[16:17], 0, s[6:7]
	v_bfe_u32 v15, v6, 16, 1
	v_add_co_u32_e32 v16, vcc, s16, v16
	v_add_f32_e32 v14, v130, v14
	v_add3_u32 v15, v6, v15, s15
	v_addc_co_u32_e32 v17, vcc, 0, v17, vcc
	global_store_short_d16_hi v[16:17], v15, off offset:512
	v_bfe_u32 v15, v14, 16, 1
	v_add3_u32 v15, v14, v15, s15
	global_store_short_d16_hi v[18:19], v15, off offset:128
	v_pk_mul_f32 v[14:15], v[12:13], v[14:15] op_sel_hi:[1,0]
	v_lshl_add_u64 v[16:17], s[94:95], 0, v[72:73]
	v_pk_fma_f32 v[20:21], v[10:11], v[6:7], v[14:15] neg_lo:[0,0,1] neg_hi:[0,0,1]
	v_pk_fma_f32 v[14:15], v[10:11], v[6:7], v[14:15] op_sel_hi:[1,0,1]
	v_lshl_add_u64 v[16:17], v[16:17], 0, v[8:9]
	v_mov_b32_e32 v21, v15
	v_pk_add_f32 v[14:15], v[64:65], v[20:21]
	v_lshl_add_u64 v[18:19], v[16:17], 0, s[6:7]
	v_bfe_u32 v6, v14, 16, 1
	v_add_co_u32_e32 v16, vcc, s16, v16
	v_add3_u32 v6, v14, v6, s15
	s_nop 0
	v_addc_co_u32_e32 v17, vcc, 0, v17, vcc
	global_store_short_d16_hi v[16:17], v6, off offset:512
	v_bfe_u32 v6, v15, 16, 1
	v_add3_u32 v6, v15, v6, s15
	v_pk_mul_f32 v[16:17], v[10:11], v[14:15]
	global_store_short_d16_hi v[18:19], v6, off offset:128
	v_sub_f32_e32 v6, v16, v17
	v_lshl_add_u64 v[16:17], s[94:95], 0, v[74:75]
	s_waitcnt vmcnt(62)
	v_add_f32_e32 v6, v133, v6
	v_pk_mul_f32 v[14:15], v[10:11], v[14:15] op_sel:[0,1] op_sel_hi:[1,0]
	v_lshl_add_u64 v[16:17], v[16:17], 0, v[8:9]
	v_add_f32_e32 v14, v14, v15
	v_lshl_add_u64 v[18:19], v[16:17], 0, s[6:7]
	v_bfe_u32 v15, v6, 16, 1
	v_add_co_u32_e32 v16, vcc, s16, v16
	v_add_f32_e32 v14, v132, v14
	v_add3_u32 v15, v6, v15, s15
	v_addc_co_u32_e32 v17, vcc, 0, v17, vcc
	global_store_short_d16_hi v[16:17], v15, off offset:512
	v_bfe_u32 v15, v14, 16, 1
	v_add3_u32 v15, v14, v15, s15
	global_store_short_d16_hi v[18:19], v15, off offset:128
	v_pk_mul_f32 v[14:15], v[12:13], v[14:15] op_sel_hi:[1,0]
	v_lshl_add_u64 v[16:17], s[94:95], 0, v[78:79]
	v_pk_fma_f32 v[20:21], v[10:11], v[6:7], v[14:15] neg_lo:[0,0,1] neg_hi:[0,0,1]
	v_pk_fma_f32 v[14:15], v[10:11], v[6:7], v[14:15] op_sel_hi:[1,0,1]
	v_lshl_add_u64 v[16:17], v[16:17], 0, v[8:9]
	v_mov_b32_e32 v21, v15
	v_pk_add_f32 v[14:15], v[70:71], v[20:21]
	v_lshl_add_u64 v[18:19], v[16:17], 0, s[6:7]
	v_bfe_u32 v6, v14, 16, 1
	v_add_co_u32_e32 v16, vcc, s16, v16
	v_add3_u32 v6, v14, v6, s15
	s_nop 0
	v_addc_co_u32_e32 v17, vcc, 0, v17, vcc
	global_store_short_d16_hi v[16:17], v6, off offset:512
	v_bfe_u32 v6, v15, 16, 1
	v_add3_u32 v6, v15, v6, s15
	v_pk_mul_f32 v[16:17], v[10:11], v[14:15]
	global_store_short_d16_hi v[18:19], v6, off offset:128
	v_sub_f32_e32 v6, v16, v17
	v_lshl_add_u64 v[16:17], s[94:95], 0, v[80:81]
	s_waitcnt vmcnt(62)
	v_add_f32_e32 v6, v135, v6
	v_pk_mul_f32 v[14:15], v[10:11], v[14:15] op_sel:[0,1] op_sel_hi:[1,0]
	v_lshl_add_u64 v[16:17], v[16:17], 0, v[8:9]
	v_add_f32_e32 v14, v14, v15
	v_lshl_add_u64 v[18:19], v[16:17], 0, s[6:7]
	v_bfe_u32 v15, v6, 16, 1
	v_add_co_u32_e32 v16, vcc, s16, v16
	v_add_f32_e32 v14, v134, v14
	v_add3_u32 v15, v6, v15, s15
	v_addc_co_u32_e32 v17, vcc, 0, v17, vcc
	global_store_short_d16_hi v[16:17], v15, off offset:512
	v_bfe_u32 v15, v14, 16, 1
	v_add3_u32 v15, v14, v15, s15
	global_store_short_d16_hi v[18:19], v15, off offset:128
	v_pk_mul_f32 v[14:15], v[12:13], v[14:15] op_sel_hi:[1,0]
	v_lshl_add_u64 v[16:17], s[94:95], 0, v[84:85]
	v_pk_fma_f32 v[20:21], v[10:11], v[6:7], v[14:15] neg_lo:[0,0,1] neg_hi:[0,0,1]
	v_pk_fma_f32 v[14:15], v[10:11], v[6:7], v[14:15] op_sel_hi:[1,0,1]
	v_lshl_add_u64 v[16:17], v[16:17], 0, v[8:9]
	v_mov_b32_e32 v21, v15
	v_pk_add_f32 v[14:15], v[76:77], v[20:21]
	v_lshl_add_u64 v[18:19], v[16:17], 0, s[6:7]
	v_bfe_u32 v6, v14, 16, 1
	v_add_co_u32_e32 v16, vcc, s16, v16
	v_add3_u32 v6, v14, v6, s15
	s_nop 0
	v_addc_co_u32_e32 v17, vcc, 0, v17, vcc
	global_store_short_d16_hi v[16:17], v6, off offset:512
	v_bfe_u32 v6, v15, 16, 1
	v_add3_u32 v6, v15, v6, s15
	v_pk_mul_f32 v[16:17], v[10:11], v[14:15]
	global_store_short_d16_hi v[18:19], v6, off offset:128
	v_sub_f32_e32 v6, v16, v17
	v_lshl_add_u64 v[16:17], s[94:95], 0, v[86:87]
	s_waitcnt vmcnt(62)
	v_add_f32_e32 v6, v137, v6
	v_pk_mul_f32 v[14:15], v[10:11], v[14:15] op_sel:[0,1] op_sel_hi:[1,0]
	v_lshl_add_u64 v[16:17], v[16:17], 0, v[8:9]
	v_add_f32_e32 v14, v14, v15
	v_lshl_add_u64 v[18:19], v[16:17], 0, s[6:7]
	v_bfe_u32 v15, v6, 16, 1
	v_add_co_u32_e32 v16, vcc, s16, v16
	v_add_f32_e32 v14, v136, v14
	v_add3_u32 v15, v6, v15, s15
	v_addc_co_u32_e32 v17, vcc, 0, v17, vcc
	global_store_short_d16_hi v[16:17], v15, off offset:512
	v_bfe_u32 v15, v14, 16, 1
	v_add3_u32 v15, v14, v15, s15
	global_store_short_d16_hi v[18:19], v15, off offset:128
	v_pk_mul_f32 v[14:15], v[12:13], v[14:15] op_sel_hi:[1,0]
	v_lshl_add_u64 v[16:17], s[94:95], 0, v[90:91]
	v_pk_fma_f32 v[20:21], v[10:11], v[6:7], v[14:15] neg_lo:[0,0,1] neg_hi:[0,0,1]
	v_pk_fma_f32 v[14:15], v[10:11], v[6:7], v[14:15] op_sel_hi:[1,0,1]
	v_lshl_add_u64 v[16:17], v[16:17], 0, v[8:9]
	v_mov_b32_e32 v21, v15
	v_pk_add_f32 v[14:15], v[82:83], v[20:21]
	v_lshl_add_u64 v[18:19], v[16:17], 0, s[6:7]
	v_bfe_u32 v6, v14, 16, 1
	v_add_co_u32_e32 v16, vcc, s16, v16
	v_add3_u32 v6, v14, v6, s15
	s_nop 0
	v_addc_co_u32_e32 v17, vcc, 0, v17, vcc
	global_store_short_d16_hi v[16:17], v6, off offset:512
	v_bfe_u32 v6, v15, 16, 1
	v_add3_u32 v6, v15, v6, s15
	v_pk_mul_f32 v[16:17], v[10:11], v[14:15]
	global_store_short_d16_hi v[18:19], v6, off offset:128
	v_sub_f32_e32 v6, v16, v17
	v_lshl_add_u64 v[16:17], s[94:95], 0, v[92:93]
	s_waitcnt vmcnt(62)
	v_add_f32_e32 v6, v139, v6
	v_pk_mul_f32 v[14:15], v[10:11], v[14:15] op_sel:[0,1] op_sel_hi:[1,0]
	v_lshl_add_u64 v[16:17], v[16:17], 0, v[8:9]
	v_add_f32_e32 v14, v14, v15
	v_lshl_add_u64 v[18:19], v[16:17], 0, s[6:7]
	v_bfe_u32 v15, v6, 16, 1
	v_add_co_u32_e32 v16, vcc, s16, v16
	v_add_f32_e32 v14, v138, v14
	v_add3_u32 v15, v6, v15, s15
	v_addc_co_u32_e32 v17, vcc, 0, v17, vcc
	global_store_short_d16_hi v[16:17], v15, off offset:512
	v_bfe_u32 v15, v14, 16, 1
	v_add3_u32 v15, v14, v15, s15
	global_store_short_d16_hi v[18:19], v15, off offset:128
	v_pk_mul_f32 v[14:15], v[12:13], v[14:15] op_sel_hi:[1,0]
	v_lshl_add_u64 v[16:17], s[94:95], 0, v[96:97]
	v_pk_fma_f32 v[20:21], v[10:11], v[6:7], v[14:15] neg_lo:[0,0,1] neg_hi:[0,0,1]
	v_pk_fma_f32 v[14:15], v[10:11], v[6:7], v[14:15] op_sel_hi:[1,0,1]
	v_lshl_add_u64 v[16:17], v[16:17], 0, v[8:9]
	v_mov_b32_e32 v21, v15
	v_pk_add_f32 v[14:15], v[88:89], v[20:21]
	v_lshl_add_u64 v[18:19], v[16:17], 0, s[6:7]
	v_bfe_u32 v6, v14, 16, 1
	v_add_co_u32_e32 v16, vcc, s16, v16
	v_add3_u32 v6, v14, v6, s15
	s_nop 0
	v_addc_co_u32_e32 v17, vcc, 0, v17, vcc
	global_store_short_d16_hi v[16:17], v6, off offset:512
	v_bfe_u32 v6, v15, 16, 1
	v_add3_u32 v6, v15, v6, s15
	v_pk_mul_f32 v[16:17], v[10:11], v[14:15]
	global_store_short_d16_hi v[18:19], v6, off offset:128
	v_sub_f32_e32 v6, v16, v17
	v_lshl_add_u64 v[16:17], s[94:95], 0, v[98:99]
	s_waitcnt vmcnt(62)
	v_add_f32_e32 v6, v141, v6
	v_pk_mul_f32 v[14:15], v[10:11], v[14:15] op_sel:[0,1] op_sel_hi:[1,0]
	v_lshl_add_u64 v[16:17], v[16:17], 0, v[8:9]
	v_add_f32_e32 v14, v14, v15
	v_lshl_add_u64 v[18:19], v[16:17], 0, s[6:7]
	v_bfe_u32 v15, v6, 16, 1
	v_add_co_u32_e32 v16, vcc, s16, v16
	v_add_f32_e32 v14, v140, v14
	v_add3_u32 v15, v6, v15, s15
	v_addc_co_u32_e32 v17, vcc, 0, v17, vcc
	global_store_short_d16_hi v[16:17], v15, off offset:512
	v_bfe_u32 v15, v14, 16, 1
	v_add3_u32 v15, v14, v15, s15
	global_store_short_d16_hi v[18:19], v15, off offset:128
	v_pk_mul_f32 v[14:15], v[12:13], v[14:15] op_sel_hi:[1,0]
	v_lshl_add_u64 v[16:17], s[94:95], 0, v[102:103]
	v_pk_fma_f32 v[20:21], v[10:11], v[6:7], v[14:15] neg_lo:[0,0,1] neg_hi:[0,0,1]
	v_pk_fma_f32 v[14:15], v[10:11], v[6:7], v[14:15] op_sel_hi:[1,0,1]
	v_lshl_add_u64 v[16:17], v[16:17], 0, v[8:9]
	v_mov_b32_e32 v21, v15
	v_pk_add_f32 v[14:15], v[94:95], v[20:21]
	v_lshl_add_u64 v[18:19], v[16:17], 0, s[6:7]
	v_bfe_u32 v6, v14, 16, 1
	v_add_co_u32_e32 v16, vcc, s16, v16
	v_add3_u32 v6, v14, v6, s15
	s_nop 0
	v_addc_co_u32_e32 v17, vcc, 0, v17, vcc
	global_store_short_d16_hi v[16:17], v6, off offset:512
	v_bfe_u32 v6, v15, 16, 1
	v_add3_u32 v6, v15, v6, s15
	v_pk_mul_f32 v[16:17], v[10:11], v[14:15]
	global_store_short_d16_hi v[18:19], v6, off offset:128
	v_sub_f32_e32 v6, v16, v17
	v_lshl_add_u64 v[16:17], s[94:95], 0, v[104:105]
	s_waitcnt vmcnt(62)
	v_add_f32_e32 v6, v143, v6
	v_pk_mul_f32 v[14:15], v[10:11], v[14:15] op_sel:[0,1] op_sel_hi:[1,0]
	v_lshl_add_u64 v[16:17], v[16:17], 0, v[8:9]
	v_add_f32_e32 v14, v14, v15
	v_lshl_add_u64 v[18:19], v[16:17], 0, s[6:7]
	v_bfe_u32 v15, v6, 16, 1
	v_add_co_u32_e32 v16, vcc, s16, v16
	v_add_f32_e32 v14, v142, v14
	v_add3_u32 v15, v6, v15, s15
	v_addc_co_u32_e32 v17, vcc, 0, v17, vcc
	global_store_short_d16_hi v[16:17], v15, off offset:512
	v_bfe_u32 v15, v14, 16, 1
	v_add3_u32 v15, v14, v15, s15
	global_store_short_d16_hi v[18:19], v15, off offset:128
	v_pk_mul_f32 v[14:15], v[12:13], v[14:15] op_sel_hi:[1,0]
	v_lshl_add_u64 v[16:17], s[94:95], 0, v[106:107]
	v_pk_fma_f32 v[20:21], v[10:11], v[6:7], v[14:15] neg_lo:[0,0,1] neg_hi:[0,0,1]
	v_pk_fma_f32 v[14:15], v[10:11], v[6:7], v[14:15] op_sel_hi:[1,0,1]
	v_lshl_add_u64 v[16:17], v[16:17], 0, v[8:9]
	v_mov_b32_e32 v21, v15
	v_pk_add_f32 v[14:15], v[100:101], v[20:21]
	v_lshl_add_u64 v[18:19], v[16:17], 0, s[6:7]
	v_bfe_u32 v6, v14, 16, 1
	v_add_co_u32_e32 v16, vcc, s16, v16
	v_add3_u32 v6, v14, v6, s15
	s_nop 0
	v_addc_co_u32_e32 v17, vcc, 0, v17, vcc
	global_store_short_d16_hi v[16:17], v6, off offset:512
	v_bfe_u32 v6, v15, 16, 1
	v_add3_u32 v6, v15, v6, s15
	v_pk_mul_f32 v[16:17], v[10:11], v[14:15]
	global_store_short_d16_hi v[18:19], v6, off offset:128
	v_sub_f32_e32 v6, v16, v17
	v_lshl_add_u64 v[16:17], s[94:95], 0, v[110:111]
	s_waitcnt vmcnt(62)
	v_add_f32_e32 v6, v145, v6
	v_pk_mul_f32 v[14:15], v[10:11], v[14:15] op_sel:[0,1] op_sel_hi:[1,0]
	v_lshl_add_u64 v[16:17], v[16:17], 0, v[8:9]
	v_add_f32_e32 v14, v14, v15
	v_lshl_add_u64 v[18:19], v[16:17], 0, s[6:7]
	v_bfe_u32 v15, v6, 16, 1
	v_add_co_u32_e32 v16, vcc, s16, v16
	v_add_f32_e32 v14, v144, v14
	v_add3_u32 v15, v6, v15, s15
	v_addc_co_u32_e32 v17, vcc, 0, v17, vcc
	global_store_short_d16_hi v[16:17], v15, off offset:512
	v_bfe_u32 v15, v14, 16, 1
	v_add3_u32 v15, v14, v15, s15
	global_store_short_d16_hi v[18:19], v15, off offset:128
	v_pk_mul_f32 v[14:15], v[12:13], v[14:15] op_sel_hi:[1,0]
	s_sub_i32 s18, s18, 32
	v_pk_fma_f32 v[16:17], v[10:11], v[6:7], v[14:15] neg_lo:[0,0,1] neg_hi:[0,0,1]
	v_pk_fma_f32 v[14:15], v[10:11], v[6:7], v[14:15] op_sel_hi:[1,0,1]
	s_add_i32 s9, s19, 32
	v_mov_b32_e32 v17, v15
	v_pk_add_f32 v[14:15], v[108:109], v[16:17]
	s_cmpk_lt_u32 s19, 0xe0
	s_mov_b32 s19, s9
	s_cbranch_scc1 .LBB0_2077
	s_branch .LBB0_2066
